# packed vs scalar fp32: the 244 packed v_pk_mul/add/fma_f32 of the mix_unit loop (between MFMAs) split into scalar pairs, bit-identical arithmetic
# baseline (speedup 1.0000x reference)
.LBB0_385:
	s_or_b64 exec, exec, s[18:19]
	v_lshlrev_b32_e32 v75, 3, v94
	v_lshlrev_b32_e32 v114, 2, v75
	global_load_dwordx4 v[78:81], v114, s[56:57] offset:16
	global_load_dwordx4 v[82:85], v114, s[56:57]
	s_waitcnt vmcnt(0)
	v_lshlrev_b32_e32 v62, 16, v54
	v_and_b32_e32 v63, 0xffff0000, v54
	v_lshlrev_b32_e32 v64, 16, v55
	v_and_b32_e32 v65, 0xffff0000, v55
	v_lshlrev_b32_e32 v54, 16, v58
	v_and_b32_e32 v55, 0xffff0000, v58
	v_lshlrev_b32_e32 v58, 16, v59
	v_and_b32_e32 v59, 0xffff0000, v59
	v_mul_f32_e32 v76, v54, v54
	v_mul_f32_e32 v77, v55, v55
	v_lshlrev_b32_e32 v66, 16, v56
	v_and_b32_e32 v67, 0xffff0000, v56
	v_mul_f32_e32 v86, v58, v58
	v_mul_f32_e32 v87, v59, v59
	v_add_f32_e32 v56, v76, v77
	v_lshlrev_b32_e32 v68, 16, v60
	v_and_b32_e32 v69, 0xffff0000, v60
	v_add_f32_e32 v56, v86, v56
	v_mul_f32_e32 v88, v68, v68
	v_mul_f32_e32 v89, v69, v69
	v_add_f32_e32 v56, v87, v56
	v_lshlrev_b32_e32 v60, 16, v61
	v_and_b32_e32 v61, 0xffff0000, v61
	v_add_f32_e32 v56, v88, v56
	v_mul_f32_e32 v90, v60, v60
	v_mul_f32_e32 v91, v61, v61
	v_add_f32_e32 v56, v89, v56
	v_add_f32_e32 v56, v90, v56
	v_add_f32_e32 v88, v91, v56
	v_and_b32_e32 v56, 64, v228
	v_add_u32_e32 v96, 64, v56
	v_xor_b32_e32 v56, 1, v228
	v_cmp_lt_i32_e64 s[52:53], v56, v96
	v_mul_f32_e32 v76, v62, v62
	v_mul_f32_e32 v77, v63, v63
	v_lshlrev_b32_e32 v102, 16, v50
	v_cndmask_b32_e64 v56, v228, v56, s[52:53]
	v_lshlrev_b32_e32 v92, 2, v56
	ds_bpermute_b32 v89, v92, v88
	v_and_b32_e32 v103, 0xffff0000, v50
	v_mul_f32_e32 v86, v64, v64
	v_mul_f32_e32 v87, v65, v65
	v_lshlrev_b32_e32 v100, 16, v51
	v_and_b32_e32 v101, 0xffff0000, v51
	v_fma_f32 v50, v102, v102, v76
	v_fma_f32 v51, v103, v103, v77
	v_fma_f32 v86, v100, v100, v86
	v_fma_f32 v87, v101, v101, v87
	v_add_f32_e32 v50, v50, v51
	s_waitcnt lgkmcnt(0)
	v_add_f32_e32 v97, v88, v89
	v_lshlrev_b32_e32 v88, 16, v53
	v_and_b32_e32 v89, 0xffff0000, v53
	v_lshlrev_b32_e32 v98, 16, v52
	v_and_b32_e32 v99, 0xffff0000, v52
	v_mul_f32_e32 v52, v66, v66
	v_mul_f32_e32 v53, v67, v67
	v_add_f32_e32 v50, v86, v50
	v_lshlrev_b32_e32 v56, 16, v57
	v_and_b32_e32 v57, 0xffff0000, v57
	v_fma_f32 v52, v98, v98, v52
	v_fma_f32 v53, v99, v99, v53
	v_add_f32_e32 v50, v87, v50
	v_mul_f32_e32 v90, v56, v56
	v_mul_f32_e32 v91, v57, v57
	v_add_f32_e32 v50, v52, v50
	v_fma_f32 v90, v88, v88, v90
	v_fma_f32 v91, v89, v89, v91
	v_add_f32_e32 v50, v53, v50
	v_add_f32_e32 v50, v90, v50
	v_add_f32_e32 v50, v91, v50
	ds_bpermute_b32 v51, v92, v50
	v_xor_b32_e32 v104, 2, v228
	v_cmp_lt_i32_e64 s[52:53], v104, v96
	v_xor_b32_e32 v76, 8, v228
	s_movk_i32 s2, 0x190
	v_cndmask_b32_e64 v52, v228, v104, s[52:53]
	v_lshlrev_b32_e32 v52, 2, v52
	s_waitcnt lgkmcnt(0)
	v_add_f32_e32 v50, v50, v51
	ds_bpermute_b32 v51, v52, v50
	ds_bpermute_b32 v53, v52, v97
	v_xor_b32_e32 v52, 4, v228
	v_cmp_lt_i32_e64 s[52:53], v52, v96
	s_waitcnt lgkmcnt(1)
	v_add_f32_e32 v50, v50, v51
	v_cndmask_b32_e64 v52, v228, v52, s[52:53]
	v_lshlrev_b32_e32 v52, 2, v52
	ds_bpermute_b32 v51, v52, v50
	v_cmp_lt_i32_e64 s[52:53], v76, v96
	s_waitcnt lgkmcnt(1)
	v_add_f32_e32 v53, v97, v53
	ds_bpermute_b32 v52, v52, v53
	v_cndmask_b32_e64 v76, v228, v76, s[52:53]
	v_lshlrev_b32_e32 v76, 2, v76
	s_waitcnt lgkmcnt(1)
	v_add_f32_e32 v50, v50, v51
	ds_bpermute_b32 v51, v76, v50
	s_waitcnt lgkmcnt(1)
	v_add_f32_e32 v53, v53, v52
	ds_bpermute_b32 v76, v76, v53
	s_waitcnt lgkmcnt(1)
	v_add_f32_e32 v50, v50, v51
	v_fmamk_f32 v50, v50, 0x3baaaaab, v225
	v_rsq_f32_e32 v50, v50
	s_nop 0
	v_mul_f32_e32 v78, v50, v78
	v_mul_f32_e32 v79, v50, v79
	v_mul_f32_e32 v82, v82, v50
	v_mul_f32_e32 v83, v83, v50
	v_mul_f32_e32 v84, v84, v50
	v_mul_f32_e32 v85, v85, v50
	v_mul_f32_e32 v86, v78, v98
	v_mul_f32_e32 v87, v79, v99
	v_mul_f32_e32 v78, v50, v80
	v_mul_f32_e32 v79, v50, v81
	v_mul_lo_u32 v51, v95, s2
	v_mul_f32_e32 v82, v82, v102
	v_mul_f32_e32 v83, v83, v103
	v_mul_f32_e32 v84, v84, v100
	v_mul_f32_e32 v85, v85, v101
	v_mul_f32_e32 v88, v78, v88
	v_mul_f32_e32 v89, v79, v89
	v_add_u32_e32 v52, 0, v51
	v_cvt_pk_bf16_f32 v78, v82, v83
	v_cvt_pk_bf16_f32 v79, v84, v85
	v_cvt_pk_bf16_f32 v80, v86, v87
	v_cvt_pk_bf16_f32 v81, v88, v89
	v_lshl_add_u32 v77, v75, 1, v52
	ds_write_b128 v77, v[78:81]
	s_and_saveexec_b64 s[18:19], s[50:51]
	s_cbranch_execz .LBB0_387
	v_lshl_add_u64 v[82:83], s[56:57], 0, v[114:115]
	global_load_dwordx4 v[78:81], v[82:83], off offset:512
	s_nop 0
	global_load_dwordx4 v[82:85], v[82:83], off offset:528
	v_mov_b32_e32 v51, v50
	s_waitcnt vmcnt(1)
	v_mul_f32_e32 v78, v50, v78
	v_mul_f32_e32 v79, v51, v79
	v_mul_f32_e32 v80, v50, v80
	v_mul_f32_e32 v81, v51, v81
	s_waitcnt vmcnt(0)
	v_mul_f32_e32 v82, v50, v82
	v_mul_f32_e32 v83, v51, v83
	v_mul_f32_e32 v50, v50, v84
	v_mul_f32_e32 v51, v51, v85
	v_mul_f32_e32 v62, v78, v62
	v_mul_f32_e32 v63, v79, v63
	v_mul_f32_e32 v64, v80, v64
	v_mul_f32_e32 v65, v81, v65
	v_mul_f32_e32 v66, v82, v66
	v_mul_f32_e32 v67, v83, v67
	v_mul_f32_e32 v50, v50, v56
	v_mul_f32_e32 v51, v51, v57
	v_cvt_pk_bf16_f32 v62, v62, v63
	v_cvt_pk_bf16_f32 v63, v64, v65
	v_cvt_pk_bf16_f32 v64, v66, v67
	v_cvt_pk_bf16_f32 v65, v50, v51
	ds_write_b128 v77, v[62:65] offset:256
.LBB0_387:
	s_or_b64 exec, exec, s[18:19]
	s_waitcnt lgkmcnt(1)
	v_add_f32_e32 v50, v53, v76
	global_load_dwordx4 v[62:65], v114, s[20:21] offset:16
	global_load_dwordx4 v[76:79], v114, s[20:21]
	v_fmamk_f32 v50, v50, 0x3c000000, v225
	v_rsq_f32_e32 v50, v50
	s_waitcnt vmcnt(0)
	v_mul_f32_e32 v56, v50, v76
	v_mul_f32_e32 v57, v50, v77
	v_mul_f32_e32 v54, v56, v54
	v_mul_f32_e32 v55, v57, v55
	v_mul_f32_e32 v56, v50, v78
	v_mul_f32_e32 v57, v50, v79
	v_mul_f32_e32 v56, v56, v58
	v_mul_f32_e32 v57, v57, v59
	v_mul_f32_e32 v58, v50, v62
	v_mul_f32_e32 v59, v50, v63
	v_mul_f32_e32 v51, v50, v65
	v_mul_f32_e32 v50, v50, v64
	v_mul_f32_e32 v50, v50, v60
	v_mul_f32_e32 v51, v51, v61
	v_cvt_pk_bf16_f32 v54, v54, v55
	v_cvt_pk_bf16_f32 v55, v56, v57
	v_cvt_pk_bf16_f32 v57, v50, v51
	v_lshlrev_b32_e32 v50, 7, v95
	v_mul_f32_e32 v58, v58, v68
	v_mul_f32_e32 v59, v59, v69
	v_sub_u32_e32 v51, v52, v50
	v_cvt_pk_bf16_f32 v56, v58, v59
	v_lshl_add_u32 v51, v75, 1, v51
	ds_write_b128 v51, v[54:57] offset:12800
	s_and_saveexec_b64 s[18:19], s[40:41]
	s_cbranch_execz .LBB0_389
	v_lshlrev_b32_e32 v52, 16, v30
	v_and_b32_e32 v53, 0xffff0000, v30
	v_lshlrev_b32_e32 v54, 16, v31
	v_and_b32_e32 v55, 0xffff0000, v31
	v_add3_u32 v50, 0, v50, v114
	v_lshlrev_b32_e32 v30, 16, v32
	v_and_b32_e32 v31, 0xffff0000, v32
	v_lshlrev_b32_e32 v32, 16, v33
	v_and_b32_e32 v33, 0xffff0000, v33
	ds_write_b128 v50, v[52:55] offset:21504
	ds_write_b128 v50, v[30:33] offset:21520

.LBB0_399:
	v_lshlrev_b32_e32 v6, 16, v10
	v_and_b32_e32 v7, 0xffff0000, v10
	v_mul_f32_e32 v6, 0xbfb8aa3b, v6
	v_mul_f32_e32 v7, 0xbfb8aa3b, v7
	v_exp_f32_e32 v6, v6
	v_exp_f32_e32 v7, v7
	v_lshlrev_b32_e32 v10, 16, v11
	v_lshlrev_b32_e32 v8, 16, v2
	v_and_b32_e32 v9, 0xffff0000, v2
	v_mul_f32_e32 v2, 0xbfb8aa3b, v10
	v_add_f32_e32 v6, 1.0, v6
	v_add_f32_e32 v7, 1.0, v7
	v_exp_f32_e32 v2, v2
	v_rcp_f32_e32 v6, v6
	v_rcp_f32_e32 v7, v7
	v_and_b32_e32 v11, 0xffff0000, v11
	v_add_f32_e32 v2, 1.0, v2
	v_lshlrev_b32_e32 v14, 16, v12
	v_mul_f32_e32 v6, v6, v8
	v_mul_f32_e32 v7, v7, v9
	v_rcp_f32_e32 v8, v2
	v_mul_f32_e32 v2, 0xbfb8aa3b, v11
	v_exp_f32_e32 v2, v2
	v_and_b32_e32 v12, 0xffff0000, v12
	v_lshlrev_b32_e32 v15, 16, v13
	v_lshlrev_b32_e32 v10, 16, v4
	v_add_f32_e32 v2, 1.0, v2
	v_rcp_f32_e32 v9, v2
	v_lshlrev_b32_e32 v2, 16, v3
	v_and_b32_e32 v3, 0xffff0000, v3
	v_and_b32_e32 v11, 0xffff0000, v4
	v_mul_f32_e32 v8, v8, v2
	v_mul_f32_e32 v9, v9, v3
	v_mul_f32_e32 v2, 0xbfb8aa3b, v14
	v_mul_f32_e32 v3, 0xbfb8aa3b, v12
	v_exp_f32_e32 v2, v2
	v_exp_f32_e32 v3, v3
	v_mul_f32_e32 v4, 0xbfb8aa3b, v15
	v_exp_f32_e32 v4, v4
	v_add_f32_e32 v2, 1.0, v2
	v_add_f32_e32 v3, 1.0, v3
	v_rcp_f32_e32 v2, v2
	v_rcp_f32_e32 v3, v3
	v_and_b32_e32 v13, 0xffff0000, v13
	v_add_f32_e32 v4, 1.0, v4
	v_mul_f32_e32 v2, v2, v10
	v_mul_f32_e32 v3, v3, v11
	v_rcp_f32_e32 v10, v4
	v_mul_f32_e32 v4, 0xbfb8aa3b, v13
	v_exp_f32_e32 v4, v4
	s_nop 0
	v_add_f32_e32 v4, 1.0, v4
	v_rcp_f32_e32 v11, v4
	v_lshlrev_b32_e32 v4, 16, v5
	v_and_b32_e32 v5, 0xffff0000, v5
	v_mul_f32_e32 v4, v10, v4
	v_mul_f32_e32 v5, v11, v5
	v_lshlrev_b32_e32 v10, 5, v70
	v_and_b32_e32 v10, 0xfffffc00, v10
	v_add_u32_e32 v10, v30, v10
	ds_write_b128 v10, v[6:9]
	ds_write_b128 v10, v[2:5] offset:16
.LBB0_400:
	s_or_b64 exec, exec, s[0:1]
	s_ashr_i32 s0, s55, 31
	s_lshr_b32 s0, s0, 24
	s_add_i32 s0, s55, s0
	v_and_b32_e32 v91, 15, v1
	v_ashrrev_i32_e32 v88, 4, v1
	s_ashr_i32 s2, s0, 8
	v_lshlrev_b32_e32 v82, 3, v88
	v_xor_b32_e32 v98, 16, v228
	v_xor_b32_e32 v97, 32, v228
	v_lshlrev_b32_e32 v78, 2, v88
	v_or_b32_e32 v80, s90, v91
	s_mov_b64 s[18:19], -1
	s_cmp_gt_i32 s91, 3
	v_lshlrev_b32_e32 v92, 4, v88
	v_ashrrev_i32_e32 v83, 31, v82
	v_cmp_lt_i32_e64 s[0:1], v98, v96
	v_cmp_lt_i32_e32 vcc, v97, v96
	v_ashrrev_i32_e32 v79, 31, v78
	v_ashrrev_i32_e32 v81, 31, v80
	s_waitcnt lgkmcnt(0)
	s_barrier
	s_cbranch_scc0 .LBB0_402
	s_add_i32 s3, s91, -4
	s_lshl_b32 s80, s3, 7
	s_lshl_b64 s[18:19], s[80:81], 8
	s_add_u32 s18, s28, s18
	s_addc_u32 s19, s29, s19
	v_lshlrev_b32_e32 v114, 8, v91
	v_lshl_add_u64 v[2:3], s[18:19], 0, v[114:115]
	v_lshl_add_u64 v[18:19], v[82:83], 1, v[2:3]
	s_movk_i32 s17, 0x4000
	v_add_co_u32_e64 v20, s[38:39], s17, v18
	s_movk_i32 s17, 0x5000
	s_nop 0
	v_addc_co_u32_e64 v21, s[38:39], 0, v19, s[38:39]
	v_add_co_u32_e64 v22, s[38:39], s17, v18
	s_movk_i32 s17, 0x1000
	s_nop 0
	v_addc_co_u32_e64 v23, s[38:39], 0, v19, s[38:39]
	v_add_co_u32_e64 v24, s[38:39], s17, v18
	s_movk_i32 s17, 0x2000
	s_nop 0
	v_addc_co_u32_e64 v25, s[38:39], 0, v19, s[38:39]
	v_add_co_u32_e64 v60, s[38:39], s17, v18
	v_mul_u32_u24_e32 v4, 0x88, v91
	s_nop 0
	v_addc_co_u32_e64 v61, s[38:39], 0, v19, s[38:39]
	s_movk_i32 s17, 0x6000
	v_lshlrev_b32_e32 v4, 1, v4
	v_add_co_u32_e64 v58, s[38:39], s17, v18
	v_add3_u32 v89, 0, v92, v4
	s_nop 0
	v_addc_co_u32_e64 v59, s[38:39], 0, v19, s[38:39]
	s_movk_i32 s17, 0x7000
	ds_read_b128 v[26:29], v89 offset:12800
	ds_read_b128 v[30:33], v89 offset:17152
	global_load_dwordx4 v[6:9], v[18:19], off
	global_load_dwordx4 v[14:17], v[22:23], off offset:-4096
	global_load_dwordx4 v[34:37], v[60:61], off offset:-4096
	global_load_dwordx4 v[38:41], v[22:23], off
	global_load_dwordx4 v[50:53], v[60:61], off
	v_add_co_u32_e64 v84, s[38:39], s17, v18
	s_movk_i32 s17, 0x3000
	s_nop 0
	v_addc_co_u32_e64 v85, s[38:39], 0, v19, s[38:39]
	v_add_co_u32_e64 v86, s[38:39], s17, v18
	global_load_dwordx4 v[54:57], v[84:85], off offset:-4096
	s_nop 0
	v_addc_co_u32_e64 v87, s[38:39], 0, v19, s[38:39]
	global_load_dwordx4 v[70:73], v[86:87], off
	global_load_dwordx4 v[74:77], v[84:85], off
	global_load_dwordx4 v[140:143], v[18:19], off offset:64
	global_load_dwordx4 v[144:147], v[20:21], off offset:64
	global_load_dwordx4 v[148:151], v[24:25], off offset:64
	global_load_dwordx4 v[152:155], v[22:23], off offset:64
	global_load_dwordx4 v[156:159], v[60:61], off offset:64
	global_load_dwordx4 v[160:163], v[58:59], off offset:64
	global_load_dwordx4 v[164:167], v[86:87], off offset:64
	global_load_dwordx4 v[168:171], v[84:85], off offset:64
	global_load_dwordx4 v[172:175], v[18:19], off offset:128
	global_load_dwordx4 v[176:179], v[20:21], off offset:128
	global_load_dwordx4 v[180:183], v[24:25], off offset:128
	global_load_dwordx4 v[184:187], v[22:23], off offset:128
	global_load_dwordx4 v[188:191], v[60:61], off offset:128
	global_load_dwordx4 v[192:195], v[58:59], off offset:128
	global_load_dwordx4 v[196:199], v[86:87], off offset:128
	global_load_dwordx4 v[200:203], v[84:85], off offset:128
	global_load_dwordx4 v[204:207], v[18:19], off offset:192
	global_load_dwordx4 v[208:211], v[20:21], off offset:192
	global_load_dwordx4 v[212:215], v[24:25], off offset:192
	global_load_dwordx4 v[216:219], v[22:23], off offset:192
	global_load_dwordx4 v[220:223], v[60:61], off offset:192
	global_load_dwordx4 v[234:237], v[58:59], off offset:192
	global_load_dwordx4 v[238:241], v[86:87], off offset:192
	global_load_dwordx4 v[242:245], v[84:85], off offset:192
	s_ashr_i32 s17, s16, 31
	v_readlane_b32 s36, v253, 11
	v_readlane_b32 s37, v253, 12
	v_lshlrev_b32_e32 v114, 14, v91
	v_or_b32_e32 v99, 16, v91
	s_waitcnt vmcnt(31) lgkmcnt(1)
	v_mfma_f32_16x16x32_bf16 v[2:5], v[6:9], v[26:29], 0
	s_waitcnt lgkmcnt(0)
	v_mfma_f32_16x16x32_bf16 v[6:9], v[6:9], v[30:33], 0
	s_waitcnt vmcnt(30)
	v_mfma_f32_16x16x32_bf16 v[10:13], v[26:29], v[14:17], 0
	v_mfma_f32_16x16x32_bf16 v[14:17], v[30:33], v[14:17], 0
	s_waitcnt vmcnt(29)
	v_mfma_f32_16x16x32_bf16 v[42:45], v[34:37], v[26:29], 0
	v_mfma_f32_16x16x32_bf16 v[34:37], v[34:37], v[30:33], 0
	s_waitcnt vmcnt(28)
	v_mfma_f32_16x16x32_bf16 v[46:49], v[26:29], v[38:41], 0
	v_mfma_f32_16x16x32_bf16 v[38:41], v[30:33], v[38:41], 0
	s_waitcnt vmcnt(27)
	v_mfma_f32_16x16x32_bf16 v[62:65], v[50:53], v[26:29], 0
	v_mfma_f32_16x16x32_bf16 v[50:53], v[50:53], v[30:33], 0
	s_waitcnt vmcnt(26)
	v_mfma_f32_16x16x32_bf16 v[66:69], v[26:29], v[54:57], 0
	v_mfma_f32_16x16x32_bf16 v[54:57], v[30:33], v[54:57], 0
	s_waitcnt vmcnt(25)
	v_mfma_f32_16x16x32_bf16 v[100:103], v[70:73], v[26:29], 0
	v_mfma_f32_16x16x32_bf16 v[70:73], v[70:73], v[30:33], 0
	s_waitcnt vmcnt(24)
	v_mfma_f32_16x16x32_bf16 v[26:29], v[26:29], v[74:77], 0
	v_mfma_f32_16x16x32_bf16 v[30:33], v[30:33], v[74:77], 0
	ds_read_b128 v[74:77], v89 offset:12864
	ds_read_b128 v[104:107], v89 offset:17216
	s_waitcnt vmcnt(23) lgkmcnt(1)
	v_mfma_f32_16x16x32_bf16 v[2:5], v[140:143], v[74:77], v[2:5]
	s_waitcnt lgkmcnt(0)
	v_mfma_f32_16x16x32_bf16 v[6:9], v[140:143], v[104:107], v[6:9]
	s_waitcnt vmcnt(22)
	v_mfma_f32_16x16x32_bf16 v[10:13], v[74:77], v[144:147], v[10:13]
	v_mfma_f32_16x16x32_bf16 v[14:17], v[104:107], v[144:147], v[14:17]
	s_waitcnt vmcnt(21)
	v_mfma_f32_16x16x32_bf16 v[42:45], v[148:151], v[74:77], v[42:45]
	v_mfma_f32_16x16x32_bf16 v[34:37], v[148:151], v[104:107], v[34:37]
	s_waitcnt vmcnt(20)
	v_mfma_f32_16x16x32_bf16 v[46:49], v[74:77], v[152:155], v[46:49]
	v_mfma_f32_16x16x32_bf16 v[38:41], v[104:107], v[152:155], v[38:41]
	s_waitcnt vmcnt(19)
	v_mfma_f32_16x16x32_bf16 v[62:65], v[156:159], v[74:77], v[62:65]
	v_mfma_f32_16x16x32_bf16 v[50:53], v[156:159], v[104:107], v[50:53]
	s_waitcnt vmcnt(18)
	v_mfma_f32_16x16x32_bf16 v[66:69], v[74:77], v[160:163], v[66:69]
	v_mfma_f32_16x16x32_bf16 v[54:57], v[104:107], v[160:163], v[54:57]
	s_waitcnt vmcnt(17)
	v_mfma_f32_16x16x32_bf16 v[100:103], v[164:167], v[74:77], v[100:103]
	v_mfma_f32_16x16x32_bf16 v[70:73], v[164:167], v[104:107], v[70:73]
	s_waitcnt vmcnt(16)
	v_mfma_f32_16x16x32_bf16 v[74:77], v[74:77], v[168:171], v[26:29]
	v_mfma_f32_16x16x32_bf16 v[104:107], v[104:107], v[168:171], v[30:33]
	ds_read_b128 v[108:111], v89 offset:12928
	ds_read_b128 v[116:119], v89 offset:17280
	s_waitcnt vmcnt(14) lgkmcnt(1)
	v_mfma_f32_16x16x32_bf16 v[120:123], v[108:111], v[176:179], v[10:13]
	s_waitcnt lgkmcnt(0)
	v_mfma_f32_16x16x32_bf16 v[124:127], v[116:119], v[176:179], v[14:17]
	s_nop 0
	s_nop 0
	s_waitcnt vmcnt(12)
	v_mfma_f32_16x16x32_bf16 v[46:49], v[108:111], v[184:187], v[46:49]
	v_mfma_f32_16x16x32_bf16 v[136:139], v[116:119], v[184:187], v[38:41]
	v_mfma_f32_16x16x32_bf16 v[128:131], v[180:183], v[108:111], v[42:45]
	v_mfma_f32_16x16x32_bf16 v[132:135], v[180:183], v[116:119], v[34:37]
	s_waitcnt vmcnt(11)
	v_mfma_f32_16x16x32_bf16 v[10:13], v[188:191], v[108:111], v[62:65]
	s_waitcnt vmcnt(10)
	v_mfma_f32_16x16x32_bf16 v[42:45], v[108:111], v[192:195], v[66:69]
	v_mfma_f32_16x16x32_bf16 v[62:65], v[116:119], v[192:195], v[54:57]
	v_mfma_f32_16x16x32_bf16 v[2:5], v[172:175], v[108:111], v[2:5]
	v_mfma_f32_16x16x32_bf16 v[6:9], v[172:175], v[116:119], v[6:9]
	v_mfma_f32_16x16x32_bf16 v[26:29], v[188:191], v[116:119], v[50:53]
	s_waitcnt vmcnt(9)
	v_mfma_f32_16x16x32_bf16 v[14:17], v[196:199], v[108:111], v[100:103]
	v_mfma_f32_16x16x32_bf16 v[30:33], v[196:199], v[116:119], v[70:73]
	s_waitcnt vmcnt(8)
	v_mfma_f32_16x16x32_bf16 v[38:41], v[108:111], v[200:203], v[74:77]
	s_nop 0
	ds_read_b128 v[70:73], v89 offset:12992
	s_nop 0
	ds_read_b128 v[74:77], v89 offset:17344
	v_mfma_f32_16x16x32_bf16 v[66:69], v[116:119], v[200:203], v[104:107]
	s_waitcnt vmcnt(7) lgkmcnt(0)
	v_mfma_f32_16x16x32_bf16 v[18:21], v[204:207], v[74:77], v[6:9]
	s_nop 2
	v_mfma_f32_16x16x32_bf16 v[50:53], v[204:207], v[70:73], v[2:5]
	s_waitcnt vmcnt(6)
	v_mfma_f32_16x16x32_bf16 v[34:37], v[70:73], v[208:211], v[120:123]
	v_mfma_f32_16x16x32_bf16 v[2:5], v[74:77], v[208:211], v[124:127]
	s_waitcnt vmcnt(5)
	v_mfma_f32_16x16x32_bf16 v[54:57], v[212:215], v[70:73], v[128:131]
	s_nop 4
	v_cvt_pk_bf16_f32 v34, v34, v35
	v_cvt_pk_bf16_f32 v35, v36, v37
	v_cvt_pk_bf16_f32 v2, v2, v3
	v_mfma_f32_16x16x32_bf16 v[22:25], v[212:215], v[74:77], v[132:135]
	v_cvt_pk_bf16_f32 v3, v4, v5
	s_waitcnt vmcnt(4)
	v_mfma_f32_16x16x32_bf16 v[46:49], v[70:73], v[216:219], v[46:49]
	v_mfma_f32_16x16x32_bf16 v[6:9], v[74:77], v[216:219], v[136:139]
	s_nop 4
	v_cvt_pk_bf16_f32 v46, v46, v47
	v_cvt_pk_bf16_f32 v47, v48, v49
	s_waitcnt vmcnt(3)
	v_mfma_f32_16x16x32_bf16 v[58:61], v[220:223], v[70:73], v[10:13]
	v_mfma_f32_16x16x32_bf16 v[26:29], v[220:223], v[74:77], v[26:29]
	s_nop 0
	s_waitcnt vmcnt(2)
	v_mfma_f32_16x16x32_bf16 v[10:13], v[74:77], v[234:237], v[62:65]
	s_waitcnt vmcnt(1)
	v_mfma_f32_16x16x32_bf16 v[62:65], v[238:241], v[70:73], v[14:17]
	v_mfma_f32_16x16x32_bf16 v[30:33], v[238:241], v[74:77], v[30:33]
	v_lshl_add_u32 v103, v91, 7, 0
	v_lshlrev_b32_e32 v102, 5, v88
	s_waitcnt vmcnt(0)
	v_mfma_f32_16x16x32_bf16 v[14:17], v[74:77], v[242:245], v[66:69]
	v_mul_f32_e32 v76, v51, v51
	v_fmac_f32_e32 v76, v50, v50
	v_fmac_f32_e32 v76, v52, v52
	v_fmac_f32_e32 v76, v53, v53
	v_fmac_f32_e32 v76, v54, v54
	v_fmac_f32_e32 v76, v55, v55
	v_fmac_f32_e32 v76, v56, v56
	v_fmac_f32_e32 v76, v57, v57
	v_fmac_f32_e32 v76, v58, v58
	v_fmac_f32_e32 v76, v59, v59
	v_fmac_f32_e32 v76, v60, v60
	v_mfma_f32_16x16x32_bf16 v[42:45], v[70:73], v[234:237], v[42:45]
	v_fmac_f32_e32 v76, v61, v61
	v_add_u32_e32 v104, v103, v102
	v_fmac_f32_e32 v76, v62, v62
	v_mfma_f32_16x16x32_bf16 v[38:41], v[70:73], v[242:245], v[38:41]
	ds_read_b128 v[86:89], v104 offset:21504
	ds_read_b128 v[106:109], v104 offset:21520
	v_fmac_f32_e32 v76, v63, v63
	v_fmac_f32_e32 v76, v64, v64
	v_fmac_f32_e32 v76, v65, v65
	s_waitcnt lgkmcnt(1)
	v_fmac_f32_e32 v76, v86, v86
	v_fmac_f32_e32 v76, v87, v87
	v_mul_f32_e32 v68, v88, v88
	v_mul_f32_e32 v69, v89, v89
	v_cndmask_b32_e64 v66, v228, v98, s[0:1]
	v_add_f32_e32 v68, v68, v76
	v_add_f32_e32 v76, v69, v68
	s_waitcnt lgkmcnt(0)
	v_mul_f32_e32 v68, v106, v106
	v_mul_f32_e32 v69, v107, v107
	v_lshlrev_b32_e32 v100, 2, v66
	v_add_f32_e32 v68, v68, v76
	v_add_f32_e32 v76, v69, v68
	v_mul_f32_e32 v68, v108, v108
	v_mul_f32_e32 v69, v109, v109
	s_lshl_b32 s0, s2, 2
	v_add_f32_e32 v68, v68, v76
	v_add_f32_e32 v68, v69, v68
	ds_bpermute_b32 v69, v100, v68
	s_add_i32 s0, s3, s0
	s_ashr_i32 s1, s0, 31
	v_cndmask_b32_e32 v66, v228, v97, vcc
	s_lshl_b64 s[18:19], s[0:1], 13
	v_lshlrev_b32_e32 v101, 2, v66
	s_add_u32 s18, s18, s16
	s_waitcnt lgkmcnt(0)
	v_add_f32_e32 v68, v68, v69
	s_addc_u32 s3, s19, s17
	s_lshl_b64 s[0:1], s[0:1], 20
	v_readlane_b32 s19, v253, 17
	ds_bpermute_b32 v69, v101, v68
	s_add_u32 s19, s19, s0
	v_readlane_b32 s0, v253, 18
	s_addc_u32 s38, s0, s1
	s_lshl_b64 s[0:1], s[16:17], 1
	s_add_u32 s0, s19, s0
	s_addc_u32 s1, s38, s1
	v_lshlrev_b64 v[84:85], 1, v[78:79]
	v_lshl_add_u64 v[70:71], s[0:1], 0, v[84:85]
	s_waitcnt lgkmcnt(0)
	v_add_f32_e32 v68, v68, v69
	v_readlane_b32 s0, v253, 15
	v_fmamk_f32 v68, v68, 0x3c2aaaab, v225
	v_readlane_b32 s1, v253, 16
	v_lshlrev_b64 v[66:67], 2, v[78:79]
	v_rsq_f32_e32 v90, v68
	v_or_b32_e32 v68, s18, v91
	v_mov_b64_e32 v[86:87], s[0:1]
	v_lshl_add_u64 v[72:73], s[36:37], 0, v[66:67]
	v_readlane_b32 s36, v253, 13
	v_mad_u64_u32 v[68:69], s[0:1], v68, s8, v[86:87]
	v_mov_b32_e32 v108, 0xc0
	v_readlane_b32 s37, v253, 14
	v_mad_i32_i24 v69, s3, v108, v69
	v_lshl_add_u64 v[76:77], s[22:23], 0, v[66:67]
	v_lshl_add_u64 v[74:75], s[36:37], 0, v[66:67]
	v_lshl_add_u64 v[88:89], v[68:69], 0, v[84:85]
	global_load_dwordx4 v[66:69], v[76:77], off
	v_mul_f32_e32 v50, v50, v90
	v_mul_f32_e32 v51, v51, v90
	v_mul_f32_e32 v52, v52, v90
	v_mul_f32_e32 v53, v53, v90
	v_mul_f32_e32 v54, v54, v90
	v_mul_f32_e32 v55, v55, v90
	v_lshl_add_u64 v[36:37], v[70:71], 0, v[114:115]
	v_cvt_pk_bf16_f32 v38, v38, v39
	v_cvt_pk_bf16_f32 v39, v40, v41
	s_waitcnt vmcnt(0)
	v_mul_f32_e32 v50, v66, v50
	v_mul_f32_e32 v51, v67, v51
	v_mul_f32_e32 v52, v68, v52
	v_mul_f32_e32 v53, v69, v53
	v_cvt_pk_bf16_f32 v50, v50, v51
	v_cvt_pk_bf16_f32 v51, v52, v53
	global_store_dwordx2 v[88:89], v[50:51], off
	global_load_dwordx4 v[50:53], v[76:77], off offset:64
	v_sub_u32_e32 v66, v104, v92
	ds_read_b128 v[66:69], v66 offset:21568
	s_waitcnt vmcnt(0)
	v_mul_f32_e32 v50, v50, v54
	v_mul_f32_e32 v51, v51, v55
	v_mul_f32_e32 v54, v56, v90
	v_mul_f32_e32 v55, v57, v90
	v_cvt_pk_bf16_f32 v50, v50, v51
	v_mul_f32_e32 v52, v54, v52
	v_mul_f32_e32 v53, v55, v53
	v_mul_f32_e32 v54, v58, v90
	v_mul_f32_e32 v55, v59, v90
	v_cvt_pk_bf16_f32 v51, v52, v53
	global_store_dwordx2 v[88:89], v[50:51], off offset:32
	global_load_dwordx4 v[50:53], v[76:77], off offset:128
	v_add_u32_e32 v58, v103, v92
	s_waitcnt vmcnt(0)
	v_mul_f32_e32 v50, v54, v50
	v_mul_f32_e32 v51, v55, v51
	v_mul_f32_e32 v54, v60, v90
	v_mul_f32_e32 v55, v61, v90
	v_cvt_pk_bf16_f32 v50, v50, v51
	v_mul_f32_e32 v52, v54, v52
	v_mul_f32_e32 v53, v55, v53
	v_mul_f32_e32 v54, v62, v90
	v_mul_f32_e32 v55, v63, v90
	v_cvt_pk_bf16_f32 v51, v52, v53
	global_store_dwordx2 v[88:89], v[50:51], off offset:64
	global_load_dwordx4 v[50:53], v[76:77], off offset:192
	ds_read_b128 v[58:61], v58 offset:21504
	s_waitcnt lgkmcnt(0)
	v_mul_f32_e32 v58, v90, v58
	v_mul_f32_e32 v59, v90, v59
	s_waitcnt vmcnt(0)
	v_mul_f32_e32 v50, v54, v50
	v_mul_f32_e32 v51, v55, v51
	v_mul_f32_e32 v54, v64, v90
	v_mul_f32_e32 v55, v65, v90
	v_cvt_pk_bf16_f32 v50, v50, v51
	v_mul_f32_e32 v52, v54, v52
	v_mul_f32_e32 v53, v55, v53
	v_lshlrev_b64 v[54:55], 6, v[80:81]
	v_cvt_pk_bf16_f32 v51, v52, v53
	global_store_dwordx2 v[88:89], v[50:51], off offset:96
	global_load_dwordx4 v[62:65], v[76:77], off offset:256
	global_load_dwordx4 v[104:107], v[76:77], off offset:320
	v_lshl_add_u64 v[50:51], v[72:73], 0, v[54:55]
	v_lshl_add_u64 v[54:55], v[74:75], 0, v[54:55]
	global_load_dwordx4 v[50:53], v[50:51], off
	s_waitcnt vmcnt(2)
	v_mul_f32_e32 v58, v58, v62
	v_mul_f32_e32 v59, v59, v63
	global_load_dwordx4 v[54:57], v[54:55], off
	v_mul_f32_e32 v62, v90, v66
	v_mul_f32_e32 v63, v90, v67
	s_waitcnt vmcnt(2)
	v_mul_f32_e32 v62, v62, v104
	v_mul_f32_e32 v63, v63, v105
	s_waitcnt vmcnt(0)
	v_mul_f32_e32 v66, v54, v62
	v_mul_f32_e32 v67, v55, v63
	s_nop 0
	v_fma_f32 v66, v50, v58, -v66
	v_fma_f32 v67, v51, v59, -v67
	v_mul_f32_e32 v50, v50, v62
	v_mul_f32_e32 v51, v51, v63
	s_nop 0
	v_fma_f32 v50, v54, v58, v50
	v_fma_f32 v51, v55, v59, v51
	v_mul_f32_e32 v58, v90, v68
	v_mul_f32_e32 v59, v90, v69
	v_mul_f32_e32 v54, v90, v60
	v_mul_f32_e32 v55, v90, v61
	v_mul_f32_e32 v58, v58, v106
	v_mul_f32_e32 v59, v59, v107
	v_mul_f32_e32 v54, v54, v64
	v_mul_f32_e32 v55, v55, v65
	v_mul_f32_e32 v60, v56, v58
	v_mul_f32_e32 v61, v57, v59
	v_cvt_pk_bf16_f32 v50, v50, v51
	v_fma_f32 v60, v52, v54, -v60
	v_fma_f32 v61, v53, v55, -v61
	v_mul_f32_e32 v52, v52, v58
	v_mul_f32_e32 v53, v53, v59
	s_nop 0
	v_fma_f32 v52, v56, v54, v52
	v_fma_f32 v53, v57, v55, v53
	v_cvt_pk_bf16_f32 v54, v66, v67
	v_cvt_pk_bf16_f32 v55, v60, v61
	v_cvt_pk_bf16_f32 v51, v52, v53
	global_store_dwordx2 v[88:89], v[54:55], off offset:128
	global_store_dwordx2 v[88:89], v[50:51], off offset:160
	global_store_dwordx2 v[36:37], v[34:35], off
	v_or_b32_e32 v34, 0x40000, v114
	v_mov_b32_e32 v35, v115
	v_lshl_add_u64 v[48:49], v[70:71], 0, v[34:35]
	global_store_dwordx2 v[48:49], v[46:47], off
	v_cvt_pk_bf16_f32 v46, v42, v43
	v_or_b32_e32 v42, 0x80000, v114
	v_or_b32_e32 v114, 0xc0000, v114
	v_lshl_add_u64 v[40:41], v[70:71], 0, v[114:115]
	global_store_dwordx2 v[40:41], v[38:39], off
	v_mul_f32_e32 v40, v19, v19
	v_fmac_f32_e32 v40, v18, v18
	v_fmac_f32_e32 v40, v20, v20
	v_fmac_f32_e32 v40, v21, v21
	v_fmac_f32_e32 v40, v22, v22
	v_fmac_f32_e32 v40, v23, v23
	v_fmac_f32_e32 v40, v24, v24
	v_fmac_f32_e32 v40, v25, v25
	v_fmac_f32_e32 v40, v26, v26
	v_mov_b32_e32 v43, v115
	v_fmac_f32_e32 v40, v27, v27
	v_cvt_pk_bf16_f32 v47, v44, v45
	v_lshl_add_u64 v[44:45], v[70:71], 0, v[42:43]
	v_fmac_f32_e32 v40, v28, v28
	v_lshlrev_b32_e32 v38, 7, v99
	global_store_dwordx2 v[44:45], v[46:47], off
	v_fmac_f32_e32 v40, v29, v29
	v_add3_u32 v41, 0, v38, v102
	v_fmac_f32_e32 v40, v30, v30
	ds_read_b128 v[44:47], v41 offset:21504
	ds_read_b128 v[48:51], v41 offset:21520
	v_fmac_f32_e32 v40, v31, v31
	v_fmac_f32_e32 v40, v32, v32
	v_fmac_f32_e32 v40, v33, v33
	s_waitcnt lgkmcnt(1)
	v_fmac_f32_e32 v40, v44, v44
	v_fmac_f32_e32 v40, v45, v45
	v_mul_f32_e32 v38, v46, v46
	v_mul_f32_e32 v39, v47, v47
	global_load_dwordx4 v[44:47], v[76:77], off
	v_add_f32_e32 v38, v40, v38
	v_add_f32_e32 v40, v38, v39
	s_waitcnt lgkmcnt(0)
	v_mul_f32_e32 v38, v48, v48
	v_mul_f32_e32 v39, v49, v49
	s_nop 0
	v_add_f32_e32 v38, v40, v38
	v_add_f32_e32 v40, v38, v39
	v_mul_f32_e32 v38, v50, v50
	v_mul_f32_e32 v39, v51, v51
	s_nop 0
	v_add_f32_e32 v38, v40, v38
	v_add_f32_e32 v38, v38, v39
	ds_bpermute_b32 v39, v100, v38
	s_waitcnt lgkmcnt(0)
	v_add_f32_e32 v38, v38, v39
	ds_bpermute_b32 v39, v101, v38
	s_waitcnt lgkmcnt(0)
	v_add_f32_e32 v38, v38, v39
	v_fmamk_f32 v38, v38, 0x3c2aaaab, v225
	v_rsq_f32_e32 v40, v38
	v_or_b32_e32 v38, s18, v99
	v_mad_u64_u32 v[38:39], s[0:1], v38, s8, v[86:87]
	v_mul_f32_e32 v18, v18, v40
	v_mul_f32_e32 v19, v19, v40
	v_mul_f32_e32 v20, v20, v40
	v_mul_f32_e32 v21, v21, v40
	v_mad_i32_i24 v39, s3, v108, v39
	v_lshl_add_u64 v[38:39], v[38:39], 0, v[84:85]
	v_mul_f32_e32 v22, v22, v40
	v_mul_f32_e32 v23, v23, v40
	s_mov_b64 s[18:19], 0
	s_waitcnt vmcnt(0)
	v_mul_f32_e32 v18, v44, v18
	v_mul_f32_e32 v19, v45, v19
	v_mul_f32_e32 v20, v46, v20
	v_mul_f32_e32 v21, v47, v21
	v_cvt_pk_bf16_f32 v18, v18, v19
	v_cvt_pk_bf16_f32 v19, v20, v21
	global_store_dwordx2 v[38:39], v[18:19], off
	global_load_dwordx4 v[18:21], v[76:77], off offset:64
	s_waitcnt vmcnt(0)
	v_mul_f32_e32 v18, v18, v22
	v_mul_f32_e32 v19, v19, v23
	v_mul_f32_e32 v22, v24, v40
	v_mul_f32_e32 v23, v25, v40
	v_cvt_pk_bf16_f32 v18, v18, v19
	v_mul_f32_e32 v20, v22, v20
	v_mul_f32_e32 v21, v23, v21
	v_mul_f32_e32 v22, v26, v40
	v_mul_f32_e32 v23, v27, v40
	v_cvt_pk_bf16_f32 v19, v20, v21
	global_store_dwordx2 v[38:39], v[18:19], off offset:32
	global_load_dwordx4 v[18:21], v[76:77], off offset:128
	s_waitcnt vmcnt(0)
	v_mul_f32_e32 v18, v22, v18
	v_mul_f32_e32 v19, v23, v19
	v_mul_f32_e32 v22, v28, v40
	v_mul_f32_e32 v23, v29, v40
	v_cvt_pk_bf16_f32 v18, v18, v19
	v_mul_f32_e32 v20, v22, v20
	v_mul_f32_e32 v21, v23, v21
	v_mul_f32_e32 v22, v30, v40
	v_mul_f32_e32 v23, v31, v40
	v_cvt_pk_bf16_f32 v19, v20, v21
	global_store_dwordx2 v[38:39], v[18:19], off offset:64
	global_load_dwordx4 v[18:21], v[76:77], off offset:192
	s_waitcnt vmcnt(0)
	v_mul_f32_e32 v18, v22, v18
	v_mul_f32_e32 v19, v23, v19
	v_mul_f32_e32 v22, v32, v40
	v_mul_f32_e32 v23, v33, v40
	v_cvt_pk_bf16_f32 v18, v18, v19
	v_mul_f32_e32 v20, v22, v20
	v_mul_f32_e32 v21, v23, v21
	v_sub_u32_e32 v41, v41, v92
	v_cvt_pk_bf16_f32 v19, v20, v21
	global_store_dwordx2 v[38:39], v[18:19], off offset:96
	v_or_b32_e32 v18, s90, v99
	v_ashrrev_i32_e32 v19, 31, v18
	v_lshlrev_b64 v[22:23], 6, v[18:19]
	global_load_dwordx4 v[30:33], v[76:77], off offset:256
	global_load_dwordx4 v[48:51], v[76:77], off offset:320
	v_lshl_add_u64 v[18:19], v[72:73], 0, v[22:23]
	v_lshl_add_u64 v[22:23], v[74:75], 0, v[22:23]
	global_load_dwordx4 v[18:21], v[18:19], off
	ds_read_b128 v[26:29], v41 offset:21504
	ds_read_b128 v[44:47], v41 offset:21568
	global_load_dwordx4 v[22:25], v[22:23], off
	s_waitcnt lgkmcnt(1)
	v_mul_f32_e32 v26, v40, v26
	v_mul_f32_e32 v27, v40, v27
	s_waitcnt vmcnt(3)
	v_mul_f32_e32 v26, v26, v30
	v_mul_f32_e32 v27, v27, v31
	s_waitcnt lgkmcnt(0)
	v_mul_f32_e32 v30, v40, v44
	v_mul_f32_e32 v31, v40, v45
	s_waitcnt vmcnt(2)
	v_mul_f32_e32 v30, v30, v48
	v_mul_f32_e32 v31, v31, v49
	s_waitcnt vmcnt(0)
	v_mul_f32_e32 v44, v22, v30
	v_mul_f32_e32 v45, v23, v31
	s_nop 0
	v_fma_f32 v44, v18, v26, -v44
	v_fma_f32 v45, v19, v27, -v45
	v_mul_f32_e32 v18, v18, v30
	v_mul_f32_e32 v19, v19, v31
	s_nop 0
	v_fma_f32 v18, v22, v26, v18
	v_fma_f32 v19, v23, v27, v19
	v_mul_f32_e32 v26, v40, v46
	v_mul_f32_e32 v27, v40, v47
	v_mul_f32_e32 v22, v40, v28
	v_mul_f32_e32 v23, v40, v29
	v_mul_f32_e32 v26, v26, v50
	v_mul_f32_e32 v27, v27, v51
	v_mul_f32_e32 v22, v22, v32
	v_mul_f32_e32 v23, v23, v33
	v_mul_f32_e32 v28, v24, v26
	v_mul_f32_e32 v29, v25, v27
	v_cvt_pk_bf16_f32 v18, v18, v19
	v_fma_f32 v28, v20, v22, -v28
	v_fma_f32 v29, v21, v23, -v29
	v_mul_f32_e32 v20, v20, v26
	v_mul_f32_e32 v21, v21, v27
	s_nop 0
	v_fma_f32 v20, v24, v22, v20
	v_fma_f32 v21, v25, v23, v21
	v_cvt_pk_bf16_f32 v22, v44, v45
	v_cvt_pk_bf16_f32 v19, v20, v21
	v_cvt_pk_bf16_f32 v23, v28, v29
	global_store_dwordx2 v[38:39], v[18:19], off offset:160
	v_lshl_add_u64 v[18:19], v[70:71], 0, 32
	global_store_dwordx2 v[38:39], v[22:23], off offset:128
	global_store_dwordx2 v[36:37], v[2:3], off offset:32
	v_cvt_pk_bf16_f32 v2, v6, v7
	v_cvt_pk_bf16_f32 v3, v8, v9
	v_lshl_add_u64 v[4:5], v[18:19], 0, v[34:35]
	global_store_dwordx2 v[4:5], v[2:3], off
	v_cvt_pk_bf16_f32 v2, v10, v11
	v_cvt_pk_bf16_f32 v3, v12, v13
	v_lshl_add_u64 v[4:5], v[18:19], 0, v[42:43]
	global_store_dwordx2 v[4:5], v[2:3], off
	v_cvt_pk_bf16_f32 v2, v14, v15
	v_cvt_pk_bf16_f32 v3, v16, v17
	v_lshl_add_u64 v[4:5], v[18:19], 0, v[114:115]
	global_store_dwordx2 v[4:5], v[2:3], off
.LBB0_402:
	s_andn2_b64 vcc, exec, s[18:19]
	s_cbranch_vccnz .LBB0_404
	s_mul_i32 s0, s91, 0x60
	s_mul_i32 s1, s91, 0x9000
	s_mul_hi_i32 s3, s0, 0x180
	s_add_u32 s0, s26, s1
	s_addc_u32 s1, s88, s3
	v_mul_u32_u24_e32 v2, 0xc0, v91
	v_mul_u32_u24_e32 v3, 0xc8, v91
	v_lshl_add_u64 v[36:37], v[82:83], 1, s[0:1]
	v_lshlrev_b32_e32 v3, 1, v3
	v_lshlrev_b32_e32 v114, 1, v2
	v_add3_u32 v88, 0, v92, v3
	v_lshl_add_u64 v[2:3], v[36:37], 0, v[114:115]
	s_mov_b64 s[0:1], 0x1800
	v_lshl_add_u64 v[38:39], v[2:3], 0, s[0:1]
	s_movk_i32 s0, 0x1000
	v_add_co_u32_e32 v20, vcc, s0, v2
	s_movk_i32 s0, 0x3000
	s_nop 0
	v_addc_co_u32_e32 v21, vcc, 0, v3, vcc
	v_add_co_u32_e32 v64, vcc, s0, v2
	s_movk_i32 s0, 0x4000
	s_nop 0
	v_addc_co_u32_e32 v65, vcc, 0, v3, vcc
	v_add_co_u32_e32 v62, vcc, s0, v2
	s_movk_i32 s0, 0x7000
	s_nop 0
	v_addc_co_u32_e32 v63, vcc, 0, v3, vcc
	v_or_b32_e32 v114, 0x6000, v114
	v_add_co_u32_e32 v68, vcc, s0, v2
	v_lshl_add_u64 v[66:67], v[36:37], 0, v[114:115]
	s_nop 0
	v_addc_co_u32_e32 v69, vcc, 0, v3, vcc
	ds_read_b128 v[4:7], v88
	ds_read_b128 v[8:11], v88 offset:6400
	global_load_dwordx4 v[12:15], v[2:3], off
	global_load_dwordx4 v[28:31], v[64:65], off
	global_load_dwordx4 v[40:43], v[62:63], off offset:2048
	global_load_dwordx4 v[48:51], v[66:67], off
	global_load_dwordx4 v[56:59], v[68:69], off offset:2048
	v_cmp_lt_i32_e32 vcc, v98, v96
	global_load_dwordx4 v[20:23], v[20:21], off offset:2048
	global_load_dwordx4 v[140:143], v[2:3], off offset:64
	global_load_dwordx4 v[144:147], v[38:39], off offset:64
	global_load_dwordx4 v[148:151], v[64:65], off offset:64
	global_load_dwordx4 v[152:155], v[62:63], off offset:2112
	global_load_dwordx4 v[156:159], v[66:67], off offset:64
	global_load_dwordx4 v[160:163], v[68:69], off offset:2112
	global_load_dwordx4 v[164:167], v[2:3], off offset:128
	global_load_dwordx4 v[168:171], v[38:39], off offset:128
	global_load_dwordx4 v[172:175], v[64:65], off offset:128
	global_load_dwordx4 v[176:179], v[62:63], off offset:2176
	global_load_dwordx4 v[180:183], v[66:67], off offset:128
	global_load_dwordx4 v[184:187], v[68:69], off offset:2176
	global_load_dwordx4 v[188:191], v[2:3], off offset:192
	global_load_dwordx4 v[192:195], v[38:39], off offset:192
	global_load_dwordx4 v[196:199], v[64:65], off offset:192
	global_load_dwordx4 v[200:203], v[62:63], off offset:2240
	global_load_dwordx4 v[204:207], v[66:67], off offset:192
	global_load_dwordx4 v[208:211], v[68:69], off offset:2240
	global_load_dwordx4 v[212:215], v[2:3], off offset:256
	global_load_dwordx4 v[216:219], v[38:39], off offset:256
	global_load_dwordx4 v[220:223], v[66:67], off offset:256
	global_load_dwordx4 v[234:237], v[64:65], off offset:256
	global_load_dwordx4 v[238:241], v[62:63], off offset:2304
	global_load_dwordx4 v[242:245], v[68:69], off offset:2304
	s_lshl_b32 s0, s2, 2
	s_add_i32 s0, s91, s0
	s_ashr_i32 s1, s0, 31
	s_ashr_i32 s2, s16, 31
	s_lshl_b64 s[0:1], s[0:1], 13
	s_waitcnt vmcnt(29) lgkmcnt(1)
	v_mfma_f32_16x16x32_bf16 v[16:19], v[12:15], v[4:7], 0
	s_waitcnt lgkmcnt(0)
	v_mfma_f32_16x16x32_bf16 v[12:15], v[12:15], v[8:11], 0
	s_waitcnt vmcnt(24)
	v_mfma_f32_16x16x32_bf16 v[24:27], v[20:23], v[4:7], 0
	v_mfma_f32_16x16x32_bf16 v[20:23], v[20:23], v[8:11], 0
	v_mfma_f32_16x16x32_bf16 v[32:35], v[28:31], v[4:7], 0
	v_mfma_f32_16x16x32_bf16 v[28:31], v[28:31], v[8:11], 0
	v_mfma_f32_16x16x32_bf16 v[44:47], v[40:43], v[4:7], 0
	v_mfma_f32_16x16x32_bf16 v[40:43], v[40:43], v[8:11], 0
	v_mfma_f32_16x16x32_bf16 v[52:55], v[48:51], v[4:7], 0
	v_mfma_f32_16x16x32_bf16 v[48:51], v[48:51], v[8:11], 0
	v_mfma_f32_16x16x32_bf16 v[4:7], v[56:59], v[4:7], 0
	v_mfma_f32_16x16x32_bf16 v[8:11], v[56:59], v[8:11], 0
	ds_read_b128 v[56:59], v88 offset:64
	ds_read_b128 v[70:73], v88 offset:6464
	s_waitcnt vmcnt(23) lgkmcnt(1)
	v_mfma_f32_16x16x32_bf16 v[16:19], v[140:143], v[56:59], v[16:19]
	s_waitcnt lgkmcnt(0)
	v_mfma_f32_16x16x32_bf16 v[12:15], v[140:143], v[70:73], v[12:15]
	s_waitcnt vmcnt(22)
	v_mfma_f32_16x16x32_bf16 v[24:27], v[144:147], v[56:59], v[24:27]
	v_mfma_f32_16x16x32_bf16 v[20:23], v[144:147], v[70:73], v[20:23]
	s_waitcnt vmcnt(21)
	v_mfma_f32_16x16x32_bf16 v[32:35], v[148:151], v[56:59], v[32:35]
	v_mfma_f32_16x16x32_bf16 v[28:31], v[148:151], v[70:73], v[28:31]
	s_waitcnt vmcnt(20)
	v_mfma_f32_16x16x32_bf16 v[44:47], v[152:155], v[56:59], v[44:47]
	v_mfma_f32_16x16x32_bf16 v[40:43], v[152:155], v[70:73], v[40:43]
	s_waitcnt vmcnt(19)
	v_mfma_f32_16x16x32_bf16 v[52:55], v[156:159], v[56:59], v[52:55]
	v_mfma_f32_16x16x32_bf16 v[48:51], v[156:159], v[70:73], v[48:51]
	s_waitcnt vmcnt(18)
	v_mfma_f32_16x16x32_bf16 v[4:7], v[160:163], v[56:59], v[4:7]
	v_mfma_f32_16x16x32_bf16 v[8:11], v[160:163], v[70:73], v[8:11]
	global_load_dwordx4 v[140:143], v[2:3], off offset:320
	global_load_dwordx4 v[144:147], v[38:39], off offset:320
	global_load_dwordx4 v[148:151], v[64:65], off offset:320
	global_load_dwordx4 v[152:155], v[62:63], off offset:2368
	global_load_dwordx4 v[156:159], v[66:67], off offset:320
	global_load_dwordx4 v[160:163], v[68:69], off offset:2368
	ds_read_b128 v[56:59], v88 offset:128
	ds_read_b128 v[70:73], v88 offset:6528
	s_waitcnt vmcnt(23) lgkmcnt(1)
	v_mfma_f32_16x16x32_bf16 v[16:19], v[164:167], v[56:59], v[16:19]
	s_waitcnt lgkmcnt(0)
	v_mfma_f32_16x16x32_bf16 v[12:15], v[164:167], v[70:73], v[12:15]
	s_waitcnt vmcnt(22)
	v_mfma_f32_16x16x32_bf16 v[24:27], v[168:171], v[56:59], v[24:27]
	v_mfma_f32_16x16x32_bf16 v[20:23], v[168:171], v[70:73], v[20:23]
	s_waitcnt vmcnt(21)
	v_mfma_f32_16x16x32_bf16 v[32:35], v[172:175], v[56:59], v[32:35]
	v_mfma_f32_16x16x32_bf16 v[28:31], v[172:175], v[70:73], v[28:31]
	s_waitcnt vmcnt(20)
	v_mfma_f32_16x16x32_bf16 v[44:47], v[176:179], v[56:59], v[44:47]
	v_mfma_f32_16x16x32_bf16 v[40:43], v[176:179], v[70:73], v[40:43]
	s_waitcnt vmcnt(19)
	v_mfma_f32_16x16x32_bf16 v[52:55], v[180:183], v[56:59], v[52:55]
	v_mfma_f32_16x16x32_bf16 v[48:51], v[180:183], v[70:73], v[48:51]
	s_waitcnt vmcnt(18)
	v_mfma_f32_16x16x32_bf16 v[4:7], v[184:187], v[56:59], v[4:7]
	v_mfma_f32_16x16x32_bf16 v[8:11], v[184:187], v[70:73], v[8:11]
	ds_read_b128 v[56:59], v88 offset:192
	ds_read_b128 v[70:73], v88 offset:6592
	s_waitcnt vmcnt(17) lgkmcnt(1)
	v_mfma_f32_16x16x32_bf16 v[16:19], v[188:191], v[56:59], v[16:19]
	s_waitcnt lgkmcnt(0)
	v_mfma_f32_16x16x32_bf16 v[12:15], v[188:191], v[70:73], v[12:15]
	s_waitcnt vmcnt(16)
	v_mfma_f32_16x16x32_bf16 v[24:27], v[192:195], v[56:59], v[24:27]
	v_mfma_f32_16x16x32_bf16 v[20:23], v[192:195], v[70:73], v[20:23]
	s_waitcnt vmcnt(15)
	v_mfma_f32_16x16x32_bf16 v[32:35], v[196:199], v[56:59], v[32:35]
	v_mfma_f32_16x16x32_bf16 v[28:31], v[196:199], v[70:73], v[28:31]
	s_waitcnt vmcnt(14)
	v_mfma_f32_16x16x32_bf16 v[44:47], v[200:203], v[56:59], v[44:47]
	v_mfma_f32_16x16x32_bf16 v[40:43], v[200:203], v[70:73], v[40:43]
	s_waitcnt vmcnt(13)
	v_mfma_f32_16x16x32_bf16 v[84:87], v[204:207], v[56:59], v[52:55]
	s_nop 2
	ds_read_b128 v[100:103], v88 offset:256
	ds_read_b128 v[104:107], v88 offset:6656
	v_mfma_f32_16x16x32_bf16 v[48:51], v[204:207], v[70:73], v[48:51]
	s_waitcnt vmcnt(12)
	v_mfma_f32_16x16x32_bf16 v[74:77], v[208:211], v[56:59], v[4:7]
	s_nop 2
	s_waitcnt vmcnt(11) lgkmcnt(1)
	v_mfma_f32_16x16x32_bf16 v[108:111], v[212:215], v[100:103], v[16:19]
	s_waitcnt lgkmcnt(0)
	v_mfma_f32_16x16x32_bf16 v[116:119], v[212:215], v[104:107], v[12:15]
	v_mfma_f32_16x16x32_bf16 v[70:73], v[208:211], v[70:73], v[8:11]
	s_nop 2
	s_waitcnt vmcnt(10)
	v_mfma_f32_16x16x32_bf16 v[14:17], v[216:219], v[100:103], v[24:27]
	v_mfma_f32_16x16x32_bf16 v[58:61], v[216:219], v[104:107], v[20:23]
	s_waitcnt vmcnt(8)
	v_mfma_f32_16x16x32_bf16 v[22:25], v[234:237], v[100:103], v[32:35]
	v_mfma_f32_16x16x32_bf16 v[54:57], v[234:237], v[104:107], v[28:31]
	s_nop 1
	s_waitcnt vmcnt(7)
	v_mfma_f32_16x16x32_bf16 v[18:21], v[238:241], v[100:103], v[44:47]
	v_mfma_f32_16x16x32_bf16 v[26:29], v[238:241], v[104:107], v[40:43]
	v_mfma_f32_16x16x32_bf16 v[50:53], v[220:223], v[104:107], v[48:51]
	ds_read_b128 v[34:37], v88 offset:320
	s_nop 1
	ds_read_b128 v[46:49], v88 offset:6720
	s_waitcnt vmcnt(6)
	v_mfma_f32_16x16x32_bf16 v[42:45], v[242:245], v[104:107], v[70:73]
	s_nop 2
	s_waitcnt vmcnt(4) lgkmcnt(1)
	v_mfma_f32_16x16x32_bf16 v[38:41], v[144:147], v[34:37], v[14:17]
	s_waitcnt lgkmcnt(0)
	v_mfma_f32_16x16x32_bf16 v[14:17], v[144:147], v[46:49], v[58:61]
	s_nop 0
	s_waitcnt vmcnt(3)
	v_mfma_f32_16x16x32_bf16 v[58:61], v[148:151], v[34:37], v[22:25]
	v_mfma_f32_16x16x32_bf16 v[22:25], v[148:151], v[46:49], v[54:57]
	s_waitcnt vmcnt(2)
	v_mfma_f32_16x16x32_bf16 v[54:57], v[152:155], v[34:37], v[18:21]
	v_mfma_f32_16x16x32_bf16 v[18:21], v[152:155], v[46:49], v[26:29]
	v_mfma_f32_16x16x32_bf16 v[6:9], v[220:223], v[100:103], v[84:87]
	s_waitcnt vmcnt(1)
	v_mfma_f32_16x16x32_bf16 v[26:29], v[156:159], v[34:37], v[6:9]
	v_mfma_f32_16x16x32_bf16 v[6:9], v[156:159], v[46:49], v[50:53]
	s_nop 2
	v_mfma_f32_16x16x32_bf16 v[10:13], v[242:245], v[100:103], v[74:77]
	v_mfma_f32_16x16x32_bf16 v[30:33], v[140:143], v[34:37], v[108:111]
	v_mfma_f32_16x16x32_bf16 v[2:5], v[140:143], v[46:49], v[116:119]
	s_waitcnt vmcnt(0)
	v_mfma_f32_16x16x32_bf16 v[34:37], v[160:163], v[34:37], v[10:13]
	v_mfma_f32_16x16x32_bf16 v[10:13], v[160:163], v[46:49], v[42:45]
	s_nop 3
	v_mul_f32_e32 v46, v31, v31
	v_fmac_f32_e32 v46, v30, v30
	v_fmac_f32_e32 v46, v32, v32
	v_fmac_f32_e32 v46, v33, v33
	v_fmac_f32_e32 v46, v38, v38
	v_fmac_f32_e32 v46, v39, v39
	v_fmac_f32_e32 v46, v40, v40
	v_fmac_f32_e32 v46, v41, v41
	v_fmac_f32_e32 v46, v58, v58
	v_fmac_f32_e32 v46, v59, v59
	v_fmac_f32_e32 v46, v60, v60
	v_fmac_f32_e32 v46, v61, v61
	v_fmac_f32_e32 v46, v54, v54
	v_fmac_f32_e32 v46, v55, v55
	v_fmac_f32_e32 v46, v56, v56
	v_fmac_f32_e32 v46, v57, v57
	v_fmac_f32_e32 v46, v26, v26
	v_fmac_f32_e32 v46, v27, v27
	v_mul_f32_e32 v44, v28, v28
	v_mul_f32_e32 v45, v29, v29
	v_cndmask_b32_e32 v42, v228, v98, vcc
	v_add_f32_e32 v44, v44, v46
	v_add_f32_e32 v48, v45, v44
	v_mul_f32_e32 v46, v34, v34
	v_mul_f32_e32 v47, v35, v35
	v_mul_f32_e32 v44, v36, v36
	v_mul_f32_e32 v45, v37, v37
	v_add_f32_e32 v46, v46, v48
	v_add_f32_e32 v46, v47, v46
	v_add_f32_e32 v44, v44, v46
	v_lshlrev_b32_e32 v69, 2, v42
	v_add_f32_e32 v44, v45, v44
	ds_bpermute_b32 v45, v69, v44
	v_cmp_lt_i32_e32 vcc, v97, v96
	v_mov_b32_e32 v43, s2
	s_waitcnt lgkmcnt(0)
	v_add_f32_e32 v44, v44, v45
	v_cndmask_b32_e32 v42, v228, v97, vcc
	v_lshlrev_b32_e32 v86, 2, v42
	ds_bpermute_b32 v45, v86, v44
	v_or_b32_e32 v42, s16, v91
	v_lshl_add_u64 v[64:65], v[42:43], 0, s[0:1]
	v_readlane_b32 s0, v253, 11
	v_lshlrev_b64 v[42:43], 2, v[78:79]
	s_waitcnt lgkmcnt(0)
	v_add_f32_e32 v44, v44, v45
	v_fmamk_f32 v44, v44, 0x3c2aaaab, v225
	v_rsq_f32_e32 v44, v44
	v_readlane_b32 s1, v253, 12
	v_lshl_add_u64 v[62:63], s[34:35], 0, v[42:43]
	global_load_dwordx4 v[46:49], v[62:63], off offset:320
	v_lshl_add_u64 v[52:53], s[0:1], 0, v[42:43]
	v_readlane_b32 s0, v253, 13
	v_readlane_b32 s1, v253, 14
	v_mul_f32_e32 v68, 0x3e16c740, v44
	v_mul_f32_e32 v30, v30, v68
	v_mul_f32_e32 v31, v31, v68
	v_lshl_add_u64 v[50:51], s[0:1], 0, v[42:43]
	global_load_dwordx4 v[42:45], v[62:63], off
	v_mul_f32_e32 v38, v38, v68
	v_mul_f32_e32 v39, v39, v68
	v_mul_f32_e32 v34, v34, v68
	v_mul_f32_e32 v35, v35, v68
	v_mul_f32_e32 v26, v26, v68
	v_mul_f32_e32 v27, v27, v68
	v_readlane_b32 s0, v253, 19
	v_readlane_b32 s1, v253, 20
	s_waitcnt vmcnt(1)
	v_mul_f32_e32 v34, v34, v46
	v_mul_f32_e32 v35, v35, v47
	v_lshl_add_u64 v[66:67], v[78:79], 1, s[0:1]
	s_waitcnt vmcnt(0)
	v_mul_f32_e32 v72, v42, v30
	v_mul_f32_e32 v73, v43, v31
	v_mul_f32_e32 v30, v32, v68
	v_mul_f32_e32 v31, v33, v68
	s_nop 0
	v_mul_f32_e32 v70, v44, v30
	v_mul_f32_e32 v71, v45, v31
	global_load_dwordx4 v[30:33], v[62:63], off offset:64
	global_load_dwordx4 v[42:45], v[62:63], off offset:256
	s_waitcnt vmcnt(1)
	v_mul_f32_e32 v76, v30, v38
	v_mul_f32_e32 v77, v31, v39
	v_mul_f32_e32 v30, v40, v68
	v_mul_f32_e32 v31, v41, v68
	v_mul_f32_e32 v38, v58, v68
	v_mul_f32_e32 v39, v59, v68
	v_mul_f32_e32 v74, v32, v30
	v_mul_f32_e32 v75, v33, v31
	global_load_dwordx4 v[30:33], v[62:63], off offset:128
	s_waitcnt vmcnt(1)
	v_mul_f32_e32 v26, v26, v42
	v_mul_f32_e32 v27, v27, v43
	s_waitcnt vmcnt(0)
	v_mul_f32_e32 v84, v30, v38
	v_mul_f32_e32 v85, v31, v39
	v_mul_f32_e32 v30, v60, v68
	v_mul_f32_e32 v31, v61, v68
	v_mul_f32_e32 v38, v54, v68
	v_mul_f32_e32 v39, v55, v68
	v_mul_f32_e32 v58, v32, v30
	v_mul_f32_e32 v59, v33, v31
	global_load_dwordx4 v[30:33], v[62:63], off offset:192
	s_waitcnt vmcnt(0)
	v_mul_f32_e32 v60, v30, v38
	v_mul_f32_e32 v61, v31, v39
	v_mul_f32_e32 v30, v56, v68
	v_mul_f32_e32 v31, v57, v68
	v_lshlrev_b64 v[38:39], 6, v[80:81]
	v_mul_f32_e32 v54, v32, v30
	v_mul_f32_e32 v55, v33, v31
	v_lshl_add_u64 v[30:31], v[52:53], 0, v[38:39]
	v_lshl_add_u64 v[38:39], v[50:51], 0, v[38:39]
	global_load_dwordx4 v[30:33], v[30:31], off
	s_nop 0
	global_load_dwordx4 v[38:41], v[38:39], off
	s_waitcnt vmcnt(0)
	v_mul_f32_e32 v42, v34, v38
	v_mul_f32_e32 v43, v35, v39
	s_nop 0
	v_fma_f32 v42, v26, v30, -v42
	v_fma_f32 v43, v27, v31, -v43
	v_mul_f32_e32 v26, v26, v38
	v_mul_f32_e32 v27, v27, v39
	s_nop 0
	v_fma_f32 v30, v34, v30, v26
	v_fma_f32 v31, v35, v31, v27
	v_mul_f32_e32 v26, v28, v68
	v_mul_f32_e32 v27, v29, v68
	v_mul_f32_e32 v28, v36, v68
	v_mul_f32_e32 v29, v37, v68
	v_mul_f32_e32 v26, v26, v44
	v_mul_f32_e32 v27, v27, v45
	v_mul_f32_e32 v28, v28, v48
	v_mul_f32_e32 v29, v29, v49
	v_cvt_pk_bf16_f32 v30, v30, v31
	v_mul_f32_e32 v34, v28, v40
	v_mul_f32_e32 v35, v29, v41
	s_nop 0
	v_fma_f32 v34, v26, v32, -v34
	v_fma_f32 v35, v27, v33, -v35
	v_mul_f32_e32 v26, v26, v40
	v_mul_f32_e32 v27, v27, v41
	s_nop 0
	v_fma_f32 v28, v28, v32, v26
	v_fma_f32 v29, v29, v33, v27
	v_mad_u64_u32 v[26:27], s[0:1], v64, s8, v[66:67]
	v_mad_i32_i24 v27, v65, s8, v27
	v_cvt_pk_bf16_f32 v31, v28, v29
	global_store_dwordx2 v[26:27], v[30:31], off offset:160
	v_mul_f32_e32 v30, v3, v3
	v_fmac_f32_e32 v30, v2, v2
	v_fmac_f32_e32 v30, v4, v4
	v_fmac_f32_e32 v30, v5, v5
	v_fmac_f32_e32 v30, v14, v14
	v_fmac_f32_e32 v30, v15, v15
	v_fmac_f32_e32 v30, v16, v16
	v_fmac_f32_e32 v30, v17, v17
	v_fmac_f32_e32 v30, v22, v22
	v_fmac_f32_e32 v30, v23, v23
	v_fmac_f32_e32 v30, v24, v24
	v_fmac_f32_e32 v30, v25, v25
	v_fmac_f32_e32 v30, v18, v18
	v_fmac_f32_e32 v30, v19, v19
	v_cvt_pk_bf16_f32 v32, v72, v73
	v_cvt_pk_bf16_f32 v33, v70, v71
	v_fmac_f32_e32 v30, v20, v20
	global_store_dwordx2 v[26:27], v[32:33], off
	v_cvt_pk_bf16_f32 v32, v76, v77
	v_cvt_pk_bf16_f32 v33, v74, v75
	v_fmac_f32_e32 v30, v21, v21
	global_store_dwordx2 v[26:27], v[32:33], off offset:32
	v_cvt_pk_bf16_f32 v32, v84, v85
	v_cvt_pk_bf16_f32 v33, v58, v59
	v_fmac_f32_e32 v30, v6, v6
	global_store_dwordx2 v[26:27], v[32:33], off offset:64
	v_cvt_pk_bf16_f32 v32, v60, v61
	v_cvt_pk_bf16_f32 v33, v54, v55
	v_fmac_f32_e32 v30, v7, v7
	v_mul_f32_e32 v28, v8, v8
	v_mul_f32_e32 v29, v9, v9
	global_store_dwordx2 v[26:27], v[32:33], off offset:96
	v_cvt_pk_bf16_f32 v32, v42, v43
	v_cvt_pk_bf16_f32 v33, v34, v35
	v_add_f32_e32 v28, v28, v30
	global_store_dwordx2 v[26:27], v[32:33], off offset:128
	v_add_f32_e32 v32, v29, v28
	v_mul_f32_e32 v30, v10, v10
	v_mul_f32_e32 v31, v11, v11
	v_mul_f32_e32 v28, v12, v12
	v_mul_f32_e32 v29, v13, v13
	v_add_f32_e32 v30, v30, v32
	v_add_f32_e32 v30, v31, v30
	v_add_f32_e32 v28, v28, v30
	global_load_dwordx4 v[30:33], v[62:63], off
	global_load_dwordx4 v[42:45], v[62:63], off offset:320
	v_add_f32_e32 v28, v29, v28
	ds_bpermute_b32 v29, v69, v28
	s_waitcnt lgkmcnt(0)
	v_add_f32_e32 v28, v28, v29
	ds_bpermute_b32 v29, v86, v28
	s_waitcnt lgkmcnt(0)
	v_add_f32_e32 v28, v28, v29
	v_fmamk_f32 v28, v28, 0x3c2aaaab, v225
	v_rsq_f32_e32 v28, v28
	s_nop 0
	v_mul_f32_e32 v28, 0x3e16c740, v28
	v_mul_f32_e32 v2, v2, v28
	v_mul_f32_e32 v3, v3, v28
	v_mul_f32_e32 v14, v14, v28
	v_mul_f32_e32 v15, v15, v28
	v_mul_f32_e32 v10, v10, v28
	v_mul_f32_e32 v11, v11, v28
	v_mul_f32_e32 v6, v6, v28
	v_mul_f32_e32 v7, v7, v28
	s_waitcnt vmcnt(1)
	v_mul_f32_e32 v30, v30, v2
	v_mul_f32_e32 v31, v31, v3
	v_mul_f32_e32 v2, v4, v28
	v_mul_f32_e32 v3, v5, v28
	s_waitcnt vmcnt(0)
	v_mul_f32_e32 v10, v10, v42
	v_mul_f32_e32 v11, v11, v43
	v_mul_f32_e32 v32, v32, v2
	v_mul_f32_e32 v33, v33, v3
	global_load_dwordx4 v[2:5], v[62:63], off offset:64
	s_waitcnt vmcnt(0)
	v_mul_f32_e32 v34, v2, v14
	v_mul_f32_e32 v35, v3, v15
	v_mul_f32_e32 v2, v16, v28
	v_mul_f32_e32 v3, v17, v28
	v_mul_f32_e32 v14, v22, v28
	v_mul_f32_e32 v15, v23, v28
	v_mul_f32_e32 v36, v4, v2
	v_mul_f32_e32 v37, v5, v3
	global_load_dwordx4 v[2:5], v[62:63], off offset:128
	s_waitcnt vmcnt(0)
	v_mul_f32_e32 v22, v14, v2
	v_mul_f32_e32 v23, v15, v3
	v_mul_f32_e32 v2, v24, v28
	v_mul_f32_e32 v3, v25, v28
	v_mul_f32_e32 v14, v18, v28
	v_mul_f32_e32 v15, v19, v28
	v_mul_f32_e32 v24, v2, v4
	v_mul_f32_e32 v25, v3, v5
	global_load_dwordx4 v[2:5], v[62:63], off offset:192
	s_waitcnt vmcnt(0)
	v_mul_f32_e32 v38, v14, v2
	v_mul_f32_e32 v39, v15, v3
	v_mul_f32_e32 v2, v20, v28
	v_mul_f32_e32 v3, v21, v28
	global_load_dwordx4 v[18:21], v[62:63], off offset:256
	v_mul_f32_e32 v40, v2, v4
	v_mul_f32_e32 v41, v3, v5
	v_or_b32_e32 v2, 16, v80
	v_ashrrev_i32_e32 v3, 31, v2
	v_lshlrev_b64 v[14:15], 6, v[2:3]
	v_lshl_add_u64 v[2:3], v[52:53], 0, v[14:15]
	v_lshl_add_u64 v[14:15], v[50:51], 0, v[14:15]
	global_load_dwordx4 v[2:5], v[2:3], off
	s_waitcnt vmcnt(1)
	v_mul_f32_e32 v6, v6, v18
	v_mul_f32_e32 v7, v7, v19
	global_load_dwordx4 v[14:17], v[14:15], off
	s_waitcnt vmcnt(0)
	v_mul_f32_e32 v18, v10, v14
	v_mul_f32_e32 v19, v11, v15
	s_nop 0
	v_fma_f32 v18, v6, v2, -v18
	v_fma_f32 v19, v7, v3, -v19
	v_mul_f32_e32 v6, v6, v14
	v_mul_f32_e32 v7, v7, v15
	s_nop 0
	v_fma_f32 v2, v10, v2, v6
	v_fma_f32 v3, v11, v3, v7
	v_mul_f32_e32 v6, v8, v28
	v_mul_f32_e32 v7, v9, v28
	v_mul_f32_e32 v8, v12, v28
	v_mul_f32_e32 v9, v13, v28
	v_mul_f32_e32 v6, v6, v20
	v_mul_f32_e32 v7, v7, v21
	v_mul_f32_e32 v8, v8, v44
	v_mul_f32_e32 v9, v9, v45
	v_cvt_pk_bf16_f32 v2, v2, v3
	v_mul_f32_e32 v10, v8, v16
	v_mul_f32_e32 v11, v9, v17
	s_nop 0
	v_fma_f32 v10, v6, v4, -v10
	v_fma_f32 v11, v7, v5, -v11
	v_mul_f32_e32 v6, v6, v16
	v_mul_f32_e32 v7, v7, v17
	s_nop 0
	v_fma_f32 v4, v8, v4, v6
	v_fma_f32 v5, v9, v5, v7
	v_cvt_pk_bf16_f32 v6, v30, v31
	v_cvt_pk_bf16_f32 v7, v32, v33
	global_store_dwordx2 v[26:27], v[6:7], off offset:3072
	v_cvt_pk_bf16_f32 v6, v34, v35
	v_cvt_pk_bf16_f32 v7, v36, v37
	global_store_dwordx2 v[26:27], v[6:7], off offset:3104
	v_cvt_pk_bf16_f32 v6, v22, v23
	v_cvt_pk_bf16_f32 v7, v24, v25
	global_store_dwordx2 v[26:27], v[6:7], off offset:3136
	v_cvt_pk_bf16_f32 v6, v38, v39
	v_cvt_pk_bf16_f32 v7, v40, v41
	global_store_dwordx2 v[26:27], v[6:7], off offset:3168
	v_cvt_pk_bf16_f32 v6, v18, v19
	v_cvt_pk_bf16_f32 v7, v10, v11
	v_cvt_pk_bf16_f32 v3, v4, v5
	global_store_dwordx2 v[26:27], v[6:7], off offset:3200
	global_store_dwordx2 v[26:27], v[2:3], off offset:3232

.LBB0_405:
	ds_read_b128 v[16:19], v4
	ds_read_b128 v[20:23], v4 offset:16
	v_add_u32_e32 v14, -1, v14
	v_cmp_eq_u32_e32 vcc, 0, v14
	v_add_u32_e32 v4, 0xfffffc00, v4
	s_or_b64 s[0:1], vcc, s[0:1]
	s_waitcnt lgkmcnt(1)
	v_add_f32_e32 v8, v8, v16
	v_add_f32_e32 v9, v9, v17
	v_add_f32_e32 v10, v10, v18
	v_add_f32_e32 v11, v11, v19
	s_waitcnt lgkmcnt(0)
	v_add_f32_e32 v6, v6, v20
	v_add_f32_e32 v7, v7, v21
	v_add_f32_e32 v2, v2, v22
	v_add_f32_e32 v3, v3, v23
	s_andn2_b64 exec, exec, s[0:1]
	s_cbranch_execnz .LBB0_405
	s_or_b64 exec, exec, s[0:1]
	v_add3_u32 v4, v95, s16, 1
	v_min_i32_e32 v4, v4, v12
	v_cvt_f32_i32_e32 v4, v4
	v_lshlrev_b32_e32 v17, 10, v95
	v_lshlrev_b32_e32 v16, 8, v95
	v_div_scale_f32 v14, s[0:1], v4, v4, 1.0
	v_rcp_f32_e32 v15, v14
	v_div_scale_f32 v18, vcc, 1.0, v4, 1.0
	s_movk_i32 s0, 0x210
	v_fma_f32 v19, -v14, v15, 1.0
	v_fmac_f32_e32 v15, v19, v15
	v_mul_f32_e32 v19, v18, v15
	v_fma_f32 v20, -v14, v19, v18
	v_fmac_f32_e32 v19, v20, v15
	v_fma_f32 v14, -v14, v19, v18
	v_div_fmas_f32 v14, v14, v15, v19
	v_div_fixup_f32 v4, v14, v4, 1.0
	v_add3_u32 v14, 0, v17, v5
	ds_read_b128 v[18:21], v14 offset:40960
	ds_read_b128 v[22:25], v14 offset:40976
	v_mov_b32_e32 v5, v4
	v_mul_lo_u32 v15, v95, s0
	s_add_i32 s0, 0, 0x12000
	s_waitcnt lgkmcnt(1)
	v_fma_f32 v8, v4, v8, -v18
	v_fma_f32 v9, v4, v9, -v19
	s_waitcnt lgkmcnt(0)
	v_fma_f32 v2, v4, v2, -v24
	v_fma_f32 v3, v4, v3, -v25
	v_fma_f32 v10, v4, v10, -v20
	v_fma_f32 v11, v4, v11, -v21
	v_fma_f32 v18, v4, v6, -v22
	v_fma_f32 v19, v4, v7, -v23
	v_cvt_pk_bf16_f32 v6, v8, v9
	v_cvt_pk_bf16_f32 v9, v2, v3
	v_lshlrev_b32_e32 v2, 5, v94
	v_cvt_pk_bf16_f32 v7, v10, v11
	v_cvt_pk_bf16_f32 v8, v18, v19
	v_add3_u32 v15, s0, v15, v2
	v_readlane_b32 s0, v254, 27
	v_mov_b32_e32 v2, 0
	ds_write_b128 v15, v[6:9]
	v_add_u32_e32 v13, s0, v13
	s_mov_b64 s[0:1], 0
	v_mov_b32_e32 v3, v2
	v_mov_b32_e32 v6, v2
	v_mov_b32_e32 v7, v2
	v_mov_b32_e32 v8, v2
	v_mov_b32_e32 v9, v2
	v_mov_b32_e32 v10, v2
	v_mov_b32_e32 v11, v2
.LBB0_407:
	ds_read_b128 v[18:21], v13
	ds_read_b128 v[22:25], v13 offset:16
	v_add_u32_e32 v12, -1, v12
	v_cmp_eq_u32_e32 vcc, 0, v12
	v_add_u32_e32 v13, 0xfffffc00, v13
	s_or_b64 s[0:1], vcc, s[0:1]
	s_waitcnt lgkmcnt(1)
	v_add_f32_e32 v6, v6, v18
	v_add_f32_e32 v7, v7, v19
	v_add_f32_e32 v8, v8, v20
	v_add_f32_e32 v9, v9, v21
	s_waitcnt lgkmcnt(0)
	v_add_f32_e32 v10, v10, v22
	v_add_f32_e32 v11, v11, v23
	v_add_f32_e32 v2, v2, v24
	v_add_f32_e32 v3, v3, v25
	s_andn2_b64 exec, exec, s[0:1]
	s_cbranch_execnz .LBB0_407
	s_or_b64 exec, exec, s[0:1]
	ds_read_b128 v[18:21], v14 offset:40992
	ds_read_b128 v[22:25], v14 offset:41008
	v_readlane_b32 s36, v251, 20
	v_readlane_b32 s42, v251, 26
	v_readlane_b32 s43, v251, 27
	s_waitcnt lgkmcnt(1)
	v_fma_f32 v6, v4, v6, -v18
	v_fma_f32 v7, v5, v7, -v19
	v_fma_f32 v8, v4, v8, -v20
	v_fma_f32 v9, v5, v9, -v21
	s_waitcnt lgkmcnt(0)
	v_fma_f32 v10, v4, v10, -v22
	v_fma_f32 v11, v5, v11, -v23
	v_fma_f32 v12, v4, v2, -v24
	v_fma_f32 v13, v5, v3, -v25
	v_cvt_pk_bf16_f32 v2, v6, v7
	v_cvt_pk_bf16_f32 v3, v8, v9
	v_cvt_pk_bf16_f32 v4, v10, v11
	v_cvt_pk_bf16_f32 v5, v12, v13
	ds_write_b128 v15, v[2:5] offset:16
	v_or_b32_sdwa v4, v93, s54 dst_sel:DWORD dst_unused:UNUSED_PAD src0_sel:BYTE_0 src1_sel:DWORD
	v_mov_b32_e32 v5, v115
	v_mov_b32_e32 v2, 2
	v_lshl_add_u64 v[4:5], v[4:5], 2, s[42:43]
	v_lshlrev_b32_sdwa v114, v2, v93 dst_sel:DWORD dst_unused:UNUSED_PAD src0_sel:DWORD src1_sel:BYTE_0
	global_load_dword v42, v[4:5], off
	global_load_dword v50, v114, s[12:13]
	global_load_dword v51, v114, s[12:13] offset:1024
	global_load_dword v52, v114, s[12:13] offset:2048
	global_load_dword v53, v114, s[12:13] offset:3072
	v_lshl_add_u64 v[2:3], s[12:13], 0, v[114:115]
	s_movk_i32 s0, 0x1000
	v_add_co_u32_e32 v4, vcc, s0, v2
	s_movk_i32 s0, 0x2000
	s_nop 0
	v_addc_co_u32_e32 v5, vcc, 0, v3, vcc
	v_add_co_u32_e32 v6, vcc, s0, v2
	s_movk_i32 s0, 0x3000
	s_nop 0
	v_addc_co_u32_e32 v7, vcc, 0, v3, vcc
	global_load_dword v54, v[6:7], off offset:-4096
	global_load_dword v55, v[4:5], off offset:1024
	global_load_dword v56, v[4:5], off offset:2048
	global_load_dword v57, v[4:5], off offset:3072
	global_load_dword v58, v[6:7], off
	global_load_dword v59, v[6:7], off offset:1024
	global_load_dword v60, v[6:7], off offset:2048
	global_load_dword v61, v[6:7], off offset:3072
	v_add_co_u32_e32 v4, vcc, s0, v2
	s_movk_i32 s0, 0x4000
	s_nop 0
	v_addc_co_u32_e32 v5, vcc, 0, v3, vcc
	v_add_co_u32_e32 v6, vcc, s0, v2
	s_movk_i32 s0, 0x5000
	s_nop 0
	v_addc_co_u32_e32 v7, vcc, 0, v3, vcc
	global_load_dword v62, v[6:7], off offset:-4096
	global_load_dword v63, v[4:5], off offset:1024
	global_load_dword v64, v[4:5], off offset:2048
	global_load_dword v65, v[4:5], off offset:3072
	global_load_dword v66, v[6:7], off
	global_load_dword v67, v[6:7], off offset:1024
	global_load_dword v68, v[6:7], off offset:2048
	global_load_dword v69, v[6:7], off offset:3072
	v_add_co_u32_e32 v4, vcc, s0, v2
	s_movk_i32 s0, 0x6000
	s_nop 0
	v_addc_co_u32_e32 v5, vcc, 0, v3, vcc
	v_add_co_u32_e32 v6, vcc, s0, v2
	s_movk_i32 s0, 0x7000
	s_nop 0
	v_addc_co_u32_e32 v7, vcc, 0, v3, vcc
	global_load_dword v70, v[6:7], off offset:-4096
	global_load_dword v71, v[4:5], off offset:1024
	global_load_dword v72, v[4:5], off offset:2048
	global_load_dword v73, v[4:5], off offset:3072
	global_load_dword v74, v[6:7], off
	global_load_dword v75, v[6:7], off offset:1024
	global_load_dword v76, v[6:7], off offset:2048
	global_load_dword v77, v[6:7], off offset:3072
	v_add_co_u32_e32 v2, vcc, s0, v2
	v_and_b32_e32 v17, 0xfffff000, v16
	s_nop 0
	v_addc_co_u32_e32 v3, vcc, 0, v3, vcc
	global_load_dword v81, v[2:3], off
	global_load_dword v84, v[2:3], off offset:1024
	global_load_dword v85, v[2:3], off offset:2048
	v_or_b32_sdwa v2, v17, v93 dst_sel:DWORD dst_unused:UNUSED_PAD src0_sel:DWORD src1_sel:BYTE_0
	v_lshlrev_b32_e32 v43, 2, v2
	v_readlane_b32 s0, v254, 26
	v_or_b32_sdwa v16, v93, v16 dst_sel:DWORD dst_unused:UNUSED_PAD src0_sel:BYTE_0 src1_sel:DWORD
	s_ashr_i32 s18, s91, 1
	v_add_u32_e32 v18, s0, v43
	ds_read2st64_b32 v[14:15], v18 offset1:4
	ds_read2st64_b32 v[12:13], v18 offset0:8 offset1:12
	ds_read2st64_b32 v[10:11], v18 offset0:16 offset1:20
	ds_read2st64_b32 v[8:9], v18 offset0:24 offset1:28
	ds_read2st64_b32 v[6:7], v18 offset0:32 offset1:36
	ds_read2st64_b32 v[4:5], v18 offset0:40 offset1:44
	ds_read2st64_b32 v[2:3], v18 offset0:48 offset1:52
	ds_read_b32 v86, v18 offset:14336
	v_mov_b32_e32 v18, 0x3c00
	v_lshl_or_b32 v44, v16, 2, v18
	v_add_u32_e32 v16, s0, v44
	ds_read_b32 v87, v16
	v_lshlrev_b32_e32 v16, 2, v17
	v_add3_u32 v45, s0, v16, v114
	ds_read2st64_b32 v[30:31], v45 offset0:64 offset1:68
	ds_read2st64_b32 v[28:29], v45 offset0:72 offset1:76
	ds_read2st64_b32 v[26:27], v45 offset0:80 offset1:84
	ds_read2st64_b32 v[24:25], v45 offset0:88 offset1:92
	ds_read2st64_b32 v[22:23], v45 offset0:96 offset1:100
	ds_read2st64_b32 v[20:21], v45 offset0:104 offset1:108
	ds_read2st64_b32 v[16:17], v45 offset0:112 offset1:116
	ds_read2st64_b32 v[18:19], v45 offset0:120 offset1:124
	ds_read2st64_b32 v[32:33], v45 offset0:128 offset1:132
	ds_read2st64_b32 v[34:35], v45 offset0:136 offset1:140
	ds_read2st64_b32 v[36:37], v45 offset0:144 offset1:148
	ds_read2st64_b32 v[38:39], v45 offset0:152 offset1:156
	ds_read2st64_b32 v[40:41], v45 offset0:160 offset1:164
	ds_read2st64_b32 v[88:89], v45 offset0:168 offset1:172
	ds_read2st64_b32 v[48:49], v45 offset0:176 offset1:180
	s_lshl_b32 s2, s18, 12
	s_ashr_i32 s3, s2, 31
	s_lshl_b32 s0, s18, 6
	s_ashr_i32 s1, s0, 31
	s_lshl_b64 s[2:3], s[2:3], 1
	s_add_u32 s16, s24, s2
	s_addc_u32 s17, s25, s3
	v_lshlrev_b32_e32 v114, 7, v91
	s_waitcnt lgkmcnt(0)
	s_barrier
	s_lshl_b32 s2, s91, 4
	s_and_b32 s2, s2, 16
	s_lshl_b32 s3, s18, 7
	s_add_i32 s3, s3, 0
	s_add_i32 s3, s3, 0x12000
	v_readlane_b32 s37, v251, 21
	v_readlane_b32 s38, v251, 22
	v_readlane_b32 s39, v251, 23
	v_readlane_b32 s40, v251, 24
	v_readlane_b32 s41, v251, 25
	s_waitcnt vmcnt(30)
	v_fma_f32 v45, v50, v87, v42
	s_waitcnt vmcnt(29)
	v_fmac_f32_e32 v45, v51, v30
	v_fma_f32 v46, v50, v86, v42
	s_waitcnt vmcnt(28)
	v_fmac_f32_e32 v45, v52, v31
	v_fmac_f32_e32 v46, v51, v87
	s_waitcnt vmcnt(27)
	v_fmac_f32_e32 v45, v53, v28
	v_fmac_f32_e32 v46, v52, v30
	v_fmac_f32_e32 v46, v53, v31
	v_fma_f32 v47, v50, v3, v42
	s_waitcnt vmcnt(26)
	v_fmac_f32_e32 v45, v54, v29
	s_waitcnt vmcnt(25)
	v_fmac_f32_e32 v45, v55, v26
	v_fmac_f32_e32 v46, v54, v28
	s_waitcnt vmcnt(24)
	v_fmac_f32_e32 v45, v56, v27
	v_fmac_f32_e32 v46, v55, v29
	s_waitcnt vmcnt(23)
	v_fmac_f32_e32 v45, v57, v24
	v_fmac_f32_e32 v46, v56, v26
	s_waitcnt vmcnt(22)
	v_fmac_f32_e32 v45, v58, v25
	v_fmac_f32_e32 v46, v57, v27
	s_waitcnt vmcnt(21)
	v_fmac_f32_e32 v45, v59, v22
	v_fmac_f32_e32 v46, v58, v24
	s_waitcnt vmcnt(20)
	v_fmac_f32_e32 v45, v60, v23
	v_fmac_f32_e32 v46, v59, v25
	s_waitcnt vmcnt(19)
	v_fmac_f32_e32 v45, v61, v20
	v_fmac_f32_e32 v46, v60, v22
	s_waitcnt vmcnt(18)
	v_fmac_f32_e32 v45, v62, v21
	v_fmac_f32_e32 v46, v61, v23
	s_waitcnt vmcnt(17)
	v_fmac_f32_e32 v45, v63, v16
	v_fmac_f32_e32 v46, v62, v20
	s_waitcnt vmcnt(16)
	v_fmac_f32_e32 v45, v64, v17
	v_fmac_f32_e32 v46, v63, v21
	s_waitcnt vmcnt(15)
	v_fmac_f32_e32 v45, v65, v18
	v_fmac_f32_e32 v46, v64, v16
	s_waitcnt vmcnt(14)
	v_fmac_f32_e32 v45, v66, v19
	v_fmac_f32_e32 v46, v65, v17
	s_waitcnt vmcnt(13)
	v_fmac_f32_e32 v45, v67, v32
	v_fmac_f32_e32 v46, v66, v18
	s_waitcnt vmcnt(12)
	v_fmac_f32_e32 v45, v68, v33
	v_fmac_f32_e32 v46, v67, v19
	s_waitcnt vmcnt(11)
	v_fmac_f32_e32 v45, v69, v34
	v_fmac_f32_e32 v46, v68, v32
	s_waitcnt vmcnt(10)
	v_fmac_f32_e32 v45, v70, v35
	v_fmac_f32_e32 v46, v69, v33
	s_waitcnt vmcnt(9)
	v_fmac_f32_e32 v45, v71, v36
	v_fmac_f32_e32 v46, v70, v34
	s_waitcnt vmcnt(8)
	v_fmac_f32_e32 v45, v72, v37
	v_fmac_f32_e32 v46, v71, v35
	s_waitcnt vmcnt(7)
	v_fmac_f32_e32 v45, v73, v38
	v_fmac_f32_e32 v46, v72, v36
	s_waitcnt vmcnt(6)
	v_fmac_f32_e32 v45, v74, v39
	v_fmac_f32_e32 v46, v73, v37
	s_waitcnt vmcnt(5)
	v_fmac_f32_e32 v45, v75, v40
	v_fmac_f32_e32 v46, v74, v38
	s_waitcnt vmcnt(4)
	v_fmac_f32_e32 v45, v76, v41
	v_fmac_f32_e32 v46, v75, v39
	s_waitcnt vmcnt(3)
	v_fmac_f32_e32 v45, v77, v88
	v_fmac_f32_e32 v46, v76, v40
	s_waitcnt vmcnt(2)
	v_fmac_f32_e32 v45, v81, v89
	v_fmac_f32_e32 v46, v77, v41
	s_waitcnt vmcnt(1)
	v_fmac_f32_e32 v45, v84, v48
	v_fmac_f32_e32 v46, v81, v88
	s_waitcnt vmcnt(0)
	v_fmac_f32_e32 v45, v85, v49
	v_fmac_f32_e32 v46, v84, v89
	v_fma_f32 v49, v50, v5, v42
	v_fmac_f32_e32 v46, v85, v48
	v_fma_f32 v48, v50, v2, v42
	v_fmac_f32_e32 v49, v51, v2
	v_fmac_f32_e32 v48, v51, v3
	v_fmac_f32_e32 v49, v52, v3
	v_fmac_f32_e32 v47, v51, v86
	v_fmac_f32_e32 v48, v52, v86
	v_fmac_f32_e32 v49, v53, v86
	v_fmac_f32_e32 v47, v52, v87
	v_fmac_f32_e32 v48, v53, v87
	v_fmac_f32_e32 v49, v54, v87
	v_fmac_f32_e32 v47, v53, v30
	v_fmac_f32_e32 v48, v54, v30
	v_fmac_f32_e32 v49, v55, v30
	v_fmac_f32_e32 v47, v54, v31
	v_fmac_f32_e32 v48, v55, v31
	v_fmac_f32_e32 v49, v56, v31
	v_fmac_f32_e32 v47, v55, v28
	v_fmac_f32_e32 v48, v56, v28
	v_fmac_f32_e32 v49, v57, v28
	v_fmac_f32_e32 v47, v56, v29
	v_fmac_f32_e32 v48, v57, v29
	v_fmac_f32_e32 v49, v58, v29
	v_fmac_f32_e32 v47, v57, v26
	v_fmac_f32_e32 v48, v58, v26
	v_fmac_f32_e32 v49, v59, v26
	v_fmac_f32_e32 v47, v58, v27
	v_fmac_f32_e32 v48, v59, v27
	v_fmac_f32_e32 v49, v60, v27
	v_fmac_f32_e32 v47, v59, v24
	v_fmac_f32_e32 v48, v60, v24
	v_fmac_f32_e32 v49, v61, v24
	v_fmac_f32_e32 v47, v60, v25
	v_fmac_f32_e32 v48, v61, v25
	v_fmac_f32_e32 v49, v62, v25
	v_fmac_f32_e32 v47, v61, v22
	v_fmac_f32_e32 v48, v62, v22
	v_fmac_f32_e32 v49, v63, v22
	v_fmac_f32_e32 v47, v62, v23
	v_fmac_f32_e32 v48, v63, v23
	v_fmac_f32_e32 v49, v64, v23
	v_fmac_f32_e32 v47, v63, v20
	v_fmac_f32_e32 v48, v64, v20
	v_fmac_f32_e32 v49, v65, v20
	v_fmac_f32_e32 v47, v64, v21
	v_fmac_f32_e32 v48, v65, v21
	v_fmac_f32_e32 v49, v66, v21
	v_fmac_f32_e32 v47, v65, v16
	v_fmac_f32_e32 v48, v66, v16
	v_fmac_f32_e32 v49, v67, v16
	v_fmac_f32_e32 v47, v66, v17
	v_fmac_f32_e32 v48, v67, v17
	v_fmac_f32_e32 v49, v68, v17
	v_fmac_f32_e32 v47, v67, v18
	v_fmac_f32_e32 v48, v68, v18
	v_fmac_f32_e32 v49, v69, v18
	v_fmac_f32_e32 v47, v68, v19
	v_fmac_f32_e32 v48, v69, v19
	v_fmac_f32_e32 v49, v70, v19
	v_fmac_f32_e32 v47, v69, v32
	v_fmac_f32_e32 v48, v70, v32
	v_fmac_f32_e32 v49, v71, v32
	v_fmac_f32_e32 v47, v70, v33
	v_fmac_f32_e32 v48, v71, v33
	v_fmac_f32_e32 v49, v72, v33
	v_fmac_f32_e32 v47, v71, v34
	v_fmac_f32_e32 v48, v72, v34
	v_fmac_f32_e32 v49, v73, v34
	v_fmac_f32_e32 v47, v72, v35
	v_fmac_f32_e32 v48, v73, v35
	v_fmac_f32_e32 v49, v74, v35
	v_fmac_f32_e32 v47, v73, v36
	v_fmac_f32_e32 v48, v74, v36
	v_fmac_f32_e32 v49, v75, v36
	v_fmac_f32_e32 v47, v74, v37
	v_fmac_f32_e32 v48, v75, v37
	v_fmac_f32_e32 v49, v76, v37
	v_fmac_f32_e32 v47, v75, v38
	v_fmac_f32_e32 v48, v76, v38
	v_fmac_f32_e32 v49, v77, v38
	v_fmac_f32_e32 v47, v76, v39
	v_fmac_f32_e32 v48, v77, v39
	v_fmac_f32_e32 v49, v81, v39
	v_fmac_f32_e32 v47, v77, v40
	v_fmac_f32_e32 v48, v81, v40
	v_fmac_f32_e32 v49, v84, v40
	v_fmac_f32_e32 v47, v81, v41
	v_fmac_f32_e32 v48, v84, v41
	v_fmac_f32_e32 v49, v85, v41
	v_fma_f32 v41, v50, v4, v42
	v_fmac_f32_e32 v41, v51, v5
	v_fmac_f32_e32 v41, v52, v2
	v_fmac_f32_e32 v41, v53, v3
	v_fmac_f32_e32 v41, v54, v86
	v_fmac_f32_e32 v41, v55, v87
	v_fmac_f32_e32 v41, v56, v30
	v_fmac_f32_e32 v41, v57, v31
	v_fmac_f32_e32 v41, v58, v28
	v_fmac_f32_e32 v41, v59, v29
	v_fmac_f32_e32 v41, v60, v26
	v_fmac_f32_e32 v41, v61, v27
	v_fmac_f32_e32 v41, v62, v24
	v_fmac_f32_e32 v41, v63, v25
	v_fmac_f32_e32 v41, v64, v22
	v_fmac_f32_e32 v41, v65, v23
	v_fmac_f32_e32 v41, v66, v20
	v_fmac_f32_e32 v41, v67, v21
	v_fmac_f32_e32 v41, v68, v16
	v_fmac_f32_e32 v41, v69, v17
	v_fmac_f32_e32 v41, v70, v18
	v_fmac_f32_e32 v41, v71, v19
	v_fmac_f32_e32 v41, v72, v32
	v_fmac_f32_e32 v41, v73, v33
	v_fmac_f32_e32 v41, v74, v34
	v_fmac_f32_e32 v41, v75, v35
	v_fmac_f32_e32 v41, v76, v36
	v_fmac_f32_e32 v41, v77, v37
	v_fmac_f32_e32 v41, v81, v38
	v_fmac_f32_e32 v41, v84, v39
	v_fmac_f32_e32 v41, v85, v40
	v_fma_f32 v40, v50, v7, v42
	v_fmac_f32_e32 v40, v51, v4
	v_fmac_f32_e32 v40, v52, v5
	v_fmac_f32_e32 v40, v53, v2
	v_fmac_f32_e32 v40, v54, v3
	v_fmac_f32_e32 v40, v55, v86
	v_fmac_f32_e32 v40, v56, v87
	v_fmac_f32_e32 v40, v57, v30
	v_fmac_f32_e32 v40, v58, v31
	v_fmac_f32_e32 v40, v59, v28
	v_fmac_f32_e32 v40, v60, v29
	v_fmac_f32_e32 v40, v61, v26
	v_fmac_f32_e32 v40, v62, v27
	v_fmac_f32_e32 v40, v63, v24
	v_fmac_f32_e32 v40, v64, v25
	v_fmac_f32_e32 v40, v65, v22
	v_fmac_f32_e32 v40, v66, v23
	v_fmac_f32_e32 v40, v67, v20
	v_fmac_f32_e32 v40, v68, v21
	v_fmac_f32_e32 v40, v69, v16
	v_fmac_f32_e32 v40, v70, v17
	v_fmac_f32_e32 v40, v71, v18
	v_fmac_f32_e32 v40, v72, v19
	v_fmac_f32_e32 v40, v73, v32
	v_fmac_f32_e32 v40, v74, v33
	v_fmac_f32_e32 v40, v75, v34
	v_fmac_f32_e32 v40, v76, v35
	v_fmac_f32_e32 v40, v77, v36
	v_fmac_f32_e32 v40, v81, v37
	v_fmac_f32_e32 v40, v84, v38
	v_fmac_f32_e32 v40, v85, v39
	v_fma_f32 v39, v50, v6, v42
	v_fmac_f32_e32 v39, v51, v7
	v_fmac_f32_e32 v39, v52, v4
	v_fmac_f32_e32 v39, v53, v5
	v_fmac_f32_e32 v39, v54, v2
	v_fmac_f32_e32 v39, v55, v3
	v_fmac_f32_e32 v39, v56, v86
	v_fmac_f32_e32 v39, v57, v87
	v_fmac_f32_e32 v39, v58, v30
	v_fmac_f32_e32 v39, v59, v31
	v_fmac_f32_e32 v39, v60, v28
	v_fmac_f32_e32 v39, v61, v29
	v_fmac_f32_e32 v39, v62, v26
	v_fmac_f32_e32 v39, v63, v27
	v_fmac_f32_e32 v39, v64, v24
	v_fmac_f32_e32 v39, v65, v25
	v_fmac_f32_e32 v39, v66, v22
	v_fmac_f32_e32 v39, v67, v23
	v_fmac_f32_e32 v39, v68, v20
	v_fmac_f32_e32 v39, v69, v21
	v_fmac_f32_e32 v39, v70, v16
	v_fmac_f32_e32 v39, v71, v17
	v_fmac_f32_e32 v39, v72, v18
	v_fmac_f32_e32 v39, v73, v19
	v_fmac_f32_e32 v39, v74, v32
	v_fmac_f32_e32 v39, v75, v33
	v_fmac_f32_e32 v39, v76, v34
	v_fmac_f32_e32 v39, v77, v35
	v_fmac_f32_e32 v39, v81, v36
	v_fmac_f32_e32 v39, v84, v37
	v_fmac_f32_e32 v39, v85, v38
	v_fma_f32 v38, v50, v9, v42
	v_fmac_f32_e32 v38, v51, v6
	v_fmac_f32_e32 v38, v52, v7
	v_fmac_f32_e32 v38, v53, v4
	v_fmac_f32_e32 v38, v54, v5
	v_fmac_f32_e32 v38, v55, v2
	v_fmac_f32_e32 v38, v56, v3
	v_fmac_f32_e32 v38, v57, v86
	v_fmac_f32_e32 v38, v58, v87
	v_fmac_f32_e32 v38, v59, v30
	v_fmac_f32_e32 v38, v60, v31
	v_fmac_f32_e32 v38, v61, v28
	v_fmac_f32_e32 v38, v62, v29
	v_fmac_f32_e32 v38, v63, v26
	v_fmac_f32_e32 v38, v64, v27
	v_fmac_f32_e32 v38, v65, v24
	v_fmac_f32_e32 v38, v66, v25
	v_fmac_f32_e32 v38, v67, v22
	v_fmac_f32_e32 v38, v68, v23
	v_fmac_f32_e32 v38, v69, v20
	v_fmac_f32_e32 v38, v70, v21
	v_fmac_f32_e32 v38, v71, v16
	v_fmac_f32_e32 v38, v72, v17
	v_fmac_f32_e32 v38, v73, v18
	v_fmac_f32_e32 v38, v74, v19
	v_fmac_f32_e32 v38, v75, v32
	v_fmac_f32_e32 v38, v76, v33
	v_fmac_f32_e32 v38, v77, v34
	v_fmac_f32_e32 v38, v81, v35
	v_fmac_f32_e32 v38, v84, v36
	v_fmac_f32_e32 v38, v85, v37
	v_fma_f32 v37, v50, v8, v42
	v_fmac_f32_e32 v37, v51, v9
	v_fmac_f32_e32 v37, v52, v6
	v_fmac_f32_e32 v37, v53, v7
	v_fmac_f32_e32 v37, v54, v4
	v_fmac_f32_e32 v37, v55, v5
	v_fmac_f32_e32 v37, v56, v2
	v_fmac_f32_e32 v37, v57, v3
	v_fmac_f32_e32 v37, v58, v86
	v_fmac_f32_e32 v37, v59, v87
	v_fmac_f32_e32 v37, v60, v30
	v_fmac_f32_e32 v37, v61, v31
	v_fmac_f32_e32 v37, v62, v28
	v_fmac_f32_e32 v37, v63, v29
	v_fmac_f32_e32 v37, v64, v26
	v_fmac_f32_e32 v37, v65, v27
	v_fmac_f32_e32 v37, v66, v24
	v_fmac_f32_e32 v37, v67, v25
	v_fmac_f32_e32 v37, v68, v22
	v_fmac_f32_e32 v37, v69, v23
	v_fmac_f32_e32 v37, v70, v20
	v_fmac_f32_e32 v37, v71, v21
	v_fmac_f32_e32 v37, v72, v16
	v_fmac_f32_e32 v37, v73, v17
	v_fmac_f32_e32 v37, v74, v18
	v_fmac_f32_e32 v37, v75, v19
	v_fmac_f32_e32 v37, v76, v32
	v_fmac_f32_e32 v37, v77, v33
	v_fmac_f32_e32 v37, v81, v34
	v_fmac_f32_e32 v37, v84, v35
	v_fmac_f32_e32 v37, v85, v36
	v_fma_f32 v36, v50, v11, v42
	v_fmac_f32_e32 v36, v51, v8
	v_fmac_f32_e32 v36, v52, v9
	v_fmac_f32_e32 v36, v53, v6
	v_fmac_f32_e32 v36, v54, v7
	v_fmac_f32_e32 v36, v55, v4
	v_fmac_f32_e32 v36, v56, v5
	v_fmac_f32_e32 v36, v57, v2
	v_fmac_f32_e32 v36, v58, v3
	v_fmac_f32_e32 v36, v59, v86
	v_fmac_f32_e32 v36, v60, v87
	v_fmac_f32_e32 v36, v61, v30
	v_fmac_f32_e32 v36, v62, v31
	v_fmac_f32_e32 v36, v63, v28
	v_fmac_f32_e32 v36, v64, v29
	v_fmac_f32_e32 v36, v65, v26
	v_fmac_f32_e32 v36, v66, v27
	v_fmac_f32_e32 v36, v67, v24
	v_fmac_f32_e32 v36, v68, v25
	v_fmac_f32_e32 v36, v69, v22
	v_fmac_f32_e32 v36, v70, v23
	v_fmac_f32_e32 v36, v71, v20
	v_fmac_f32_e32 v36, v72, v21
	v_fmac_f32_e32 v36, v73, v16
	v_fmac_f32_e32 v36, v74, v17
	v_fmac_f32_e32 v36, v75, v18
	v_fmac_f32_e32 v36, v76, v19
	v_fmac_f32_e32 v36, v77, v32
	v_fmac_f32_e32 v36, v81, v33
	v_fmac_f32_e32 v36, v84, v34
	v_fmac_f32_e32 v36, v85, v35
	v_fma_f32 v35, v50, v10, v42
	v_fmac_f32_e32 v35, v51, v11
	v_fmac_f32_e32 v35, v52, v8
	v_fmac_f32_e32 v35, v53, v9
	v_fmac_f32_e32 v35, v54, v6
	v_fmac_f32_e32 v35, v55, v7
	v_fmac_f32_e32 v35, v56, v4
	v_fmac_f32_e32 v35, v57, v5
	v_fmac_f32_e32 v35, v58, v2
	v_fmac_f32_e32 v35, v59, v3
	v_fmac_f32_e32 v35, v60, v86
	v_fmac_f32_e32 v35, v61, v87
	v_fmac_f32_e32 v35, v62, v30
	v_fmac_f32_e32 v35, v63, v31
	v_fmac_f32_e32 v35, v64, v28
	v_fmac_f32_e32 v35, v65, v29
	v_fmac_f32_e32 v35, v66, v26
	v_fmac_f32_e32 v35, v67, v27
	v_fmac_f32_e32 v35, v68, v24
	v_fmac_f32_e32 v35, v69, v25
	v_fmac_f32_e32 v35, v70, v22
	v_fmac_f32_e32 v35, v71, v23
	v_fmac_f32_e32 v35, v72, v20
	v_fmac_f32_e32 v35, v73, v21
	v_fmac_f32_e32 v35, v74, v16
	v_fmac_f32_e32 v35, v75, v17
	v_fmac_f32_e32 v35, v76, v18
	v_fmac_f32_e32 v35, v77, v19
	v_fmac_f32_e32 v35, v81, v32
	v_fmac_f32_e32 v35, v84, v33
	v_fmac_f32_e32 v35, v85, v34
	v_fma_f32 v34, v50, v13, v42
	v_fmac_f32_e32 v34, v51, v10
	v_fmac_f32_e32 v34, v52, v11
	v_fmac_f32_e32 v34, v53, v8
	v_fmac_f32_e32 v34, v54, v9
	v_fmac_f32_e32 v34, v55, v6
	v_fmac_f32_e32 v34, v56, v7
	v_fmac_f32_e32 v34, v57, v4
	v_fmac_f32_e32 v34, v58, v5
	v_fmac_f32_e32 v34, v59, v2
	v_fmac_f32_e32 v34, v60, v3
	v_fmac_f32_e32 v34, v61, v86
	v_fmac_f32_e32 v34, v62, v87
	v_fmac_f32_e32 v34, v63, v30
	v_fmac_f32_e32 v34, v64, v31
	v_fmac_f32_e32 v34, v65, v28
	v_fmac_f32_e32 v34, v66, v29
	v_fmac_f32_e32 v34, v67, v26
	v_fmac_f32_e32 v34, v68, v27
	v_fmac_f32_e32 v34, v69, v24
	v_fmac_f32_e32 v34, v70, v25
	v_fmac_f32_e32 v34, v71, v22
	v_fmac_f32_e32 v34, v72, v23
	v_fmac_f32_e32 v34, v73, v20
	v_fmac_f32_e32 v34, v74, v21
	v_fmac_f32_e32 v34, v75, v16
	v_fmac_f32_e32 v34, v76, v17
	v_fmac_f32_e32 v34, v77, v18
	v_fmac_f32_e32 v34, v81, v19
	v_fmac_f32_e32 v34, v84, v32
	v_fmac_f32_e32 v34, v85, v33
	v_fma_f32 v33, v50, v12, v42
	v_fmac_f32_e32 v33, v51, v13
	v_fmac_f32_e32 v33, v52, v10
	v_fmac_f32_e32 v33, v53, v11
	v_fmac_f32_e32 v33, v54, v8
	v_fmac_f32_e32 v33, v55, v9
	v_fmac_f32_e32 v33, v56, v6
	v_fmac_f32_e32 v33, v57, v7
	v_fmac_f32_e32 v33, v58, v4
	v_fmac_f32_e32 v33, v59, v5
	v_fmac_f32_e32 v33, v60, v2
	v_fmac_f32_e32 v33, v61, v3
	v_fmac_f32_e32 v33, v62, v86
	v_fmac_f32_e32 v33, v63, v87
	v_fmac_f32_e32 v33, v64, v30
	v_fmac_f32_e32 v33, v65, v31
	v_fmac_f32_e32 v33, v66, v28
	v_fmac_f32_e32 v33, v67, v29
	v_fmac_f32_e32 v33, v68, v26
	v_fmac_f32_e32 v33, v69, v27
	v_fmac_f32_e32 v33, v70, v24
	v_fmac_f32_e32 v33, v71, v25
	v_fmac_f32_e32 v33, v72, v22
	v_fmac_f32_e32 v33, v73, v23
	v_fmac_f32_e32 v33, v74, v20
	v_fmac_f32_e32 v33, v75, v21
	v_fmac_f32_e32 v33, v76, v16
	v_fmac_f32_e32 v33, v77, v17
	v_fmac_f32_e32 v33, v81, v18
	v_fmac_f32_e32 v33, v84, v19
	v_fmac_f32_e32 v33, v85, v32
	v_fma_f32 v32, v50, v15, v42
	v_fmac_f32_e32 v42, v50, v14
	v_fmac_f32_e32 v42, v51, v15
	v_fmac_f32_e32 v32, v51, v12
	v_fmac_f32_e32 v42, v52, v12
	v_fmac_f32_e32 v32, v52, v13
	v_fmac_f32_e32 v42, v53, v13
	v_fmac_f32_e32 v32, v53, v10
	v_fmac_f32_e32 v42, v54, v10
	v_fmac_f32_e32 v32, v54, v11
	v_fmac_f32_e32 v42, v55, v11
	v_fmac_f32_e32 v32, v55, v8
	v_fmac_f32_e32 v42, v56, v8
	v_fmac_f32_e32 v32, v56, v9
	v_fmac_f32_e32 v42, v57, v9
	v_fmac_f32_e32 v32, v57, v6
	v_fmac_f32_e32 v42, v58, v6
	v_fmac_f32_e32 v32, v58, v7
	v_fmac_f32_e32 v42, v59, v7
	v_fmac_f32_e32 v32, v59, v4
	v_fmac_f32_e32 v42, v60, v4
	v_fmac_f32_e32 v32, v60, v5
	v_fmac_f32_e32 v42, v61, v5
	v_fmac_f32_e32 v32, v61, v2
	v_fmac_f32_e32 v42, v62, v2
	v_fmac_f32_e32 v32, v62, v3
	v_fmac_f32_e32 v42, v63, v3
	v_fmac_f32_e32 v32, v63, v86
	v_fmac_f32_e32 v42, v64, v86
	v_fmac_f32_e32 v32, v64, v87
	v_fmac_f32_e32 v42, v65, v87
	v_fmac_f32_e32 v32, v65, v30
	v_fmac_f32_e32 v42, v66, v30
	v_fmac_f32_e32 v32, v66, v31
	v_fmac_f32_e32 v42, v67, v31
	v_fmac_f32_e32 v32, v67, v28
	v_fmac_f32_e32 v42, v68, v28
	v_fmac_f32_e32 v32, v68, v29
	v_fmac_f32_e32 v42, v69, v29
	v_fmac_f32_e32 v32, v69, v26
	v_fmac_f32_e32 v42, v70, v26
	v_fmac_f32_e32 v32, v70, v27
	v_fmac_f32_e32 v42, v71, v27
	v_fmac_f32_e32 v32, v71, v24
	v_fmac_f32_e32 v42, v72, v24
	v_fmac_f32_e32 v32, v72, v25
	v_fmac_f32_e32 v42, v73, v25
	v_fmac_f32_e32 v32, v73, v22
	v_fmac_f32_e32 v42, v74, v22
	v_fmac_f32_e32 v32, v74, v23
	v_fmac_f32_e32 v42, v75, v23
	v_fmac_f32_e32 v32, v75, v20
	v_fmac_f32_e32 v42, v76, v20
	v_fmac_f32_e32 v32, v76, v21
	v_fmac_f32_e32 v42, v77, v21
	v_lshl_add_u64 v[26:27], v[82:83], 1, s[16:17]
	v_or_b32_e32 v30, 0x1000, v114
	v_mov_b32_e32 v31, v115
	v_fmac_f32_e32 v32, v77, v16
	v_fmac_f32_e32 v42, v81, v16
	v_lshl_add_u64 v[28:29], v[26:27], 0, v[114:115]
	v_lshl_add_u64 v[14:15], v[26:27], 0, v[30:31]
	v_fmac_f32_e32 v32, v81, v17
	v_fmac_f32_e32 v42, v84, v17
	global_load_dwordx4 v[6:9], v[28:29], off
	v_or_b32_e32 v2, s2, v91
	global_load_dwordx4 v[14:17], v[14:15], off
	v_mul_u32_u24_e32 v2, 0x210, v2
	v_add3_u32 v22, s3, v2, v92
	ds_read_b128 v[2:5], v22
	v_fmac_f32_e32 v32, v84, v18
	v_or_b32_e32 v114, 0x1800, v114
	v_fmac_f32_e32 v32, v85, v19
	v_fmac_f32_e32 v42, v85, v18
	s_waitcnt vmcnt(0) lgkmcnt(0)
	v_mfma_f32_16x16x32_bf16 v[18:21], v[14:17], v[2:5], 0
	v_lshl_add_u64 v[14:15], v[26:27], 0, v[114:115]
	global_load_dwordx4 v[10:13], v[28:29], off offset:2048
	ds_read_b128 v[22:25], v22 offset:64
	global_load_dwordx4 v[14:17], v[14:15], off
	v_mfma_f32_16x16x32_bf16 v[6:9], v[6:9], v[2:5], 0
	v_lshl_add_u64 v[26:27], v[26:27], 0, 64
	s_lshl_b64 s[16:17], s[0:1], 2
	s_add_u32 s16, s30, s16
	s_waitcnt vmcnt(1)
	v_mfma_f32_16x16x32_bf16 v[10:13], v[10:13], v[2:5], 0
	s_addc_u32 s17, s27, s17
	v_fmac_f32_e32 v47, v84, v88
	v_fmac_f32_e32 v47, v85, v89
	s_waitcnt vmcnt(0)
	v_mfma_f32_16x16x32_bf16 v[2:5], v[14:17], v[2:5], 0
	global_load_dwordx4 v[14:17], v[28:29], off offset:64
	v_fmac_f32_e32 v48, v85, v88
	v_readlane_b32 s44, v251, 28
	s_waitcnt vmcnt(0) lgkmcnt(0)
	v_mfma_f32_16x16x32_bf16 v[14:17], v[14:17], v[22:25], v[6:9]
	s_nop 2
	global_load_dwordx4 v[6:9], v[28:29], off offset:2112
	v_readlane_b32 s45, v251, 29
	v_readlane_b32 s46, v251, 30
	s_waitcnt vmcnt(0)
	v_mfma_f32_16x16x32_bf16 v[10:13], v[6:9], v[22:25], v[10:13]
	v_lshl_add_u64 v[6:7], v[26:27], 0, v[30:31]
	global_load_dwordx4 v[6:9], v[6:7], off
	v_readlane_b32 s47, v251, 31
	s_waitcnt vmcnt(0)
	v_mfma_f32_16x16x32_bf16 v[6:9], v[6:9], v[22:25], v[18:21]
	s_nop 2
	v_lshl_add_u64 v[18:19], v[26:27], 0, v[114:115]
	global_load_dwordx4 v[18:21], v[18:19], off
	v_readlane_b32 s48, v251, 32
	s_waitcnt vmcnt(0)
	v_mfma_f32_16x16x32_bf16 v[2:5], v[18:21], v[22:25], v[2:5]
	v_or_b32_e32 v18, s2, v80
	v_ashrrev_i32_e32 v19, 31, v18
	v_lshlrev_b64 v[18:19], 11, v[18:19]
	v_lshl_add_u64 v[18:19], s[86:87], 0, v[18:19]
	v_lshl_add_u64 v[22:23], v[78:79], 2, s[16:17]
	v_lshl_add_u64 v[24:25], s[0:1], 1, v[18:19]
	global_load_dwordx4 v[18:21], v[22:23], off
	s_lshl_b32 s0, s91, 2
	s_add_i32 s2, s0, s90
	s_ashr_i32 s3, s2, 31
	s_lshl_b64 s[2:3], s[2:3], 11
	s_add_u32 s2, s86, s2
	s_addc_u32 s3, s87, s3
	v_readlane_b32 s49, v251, 33
	v_readlane_b32 s50, v251, 34
	v_readlane_b32 s51, v251, 35
	s_waitcnt vmcnt(0)
	v_mul_f32_e32 v14, v14, v18
	v_mul_f32_e32 v15, v15, v19
	v_mul_f32_e32 v16, v16, v20
	v_mul_f32_e32 v17, v17, v21
	v_cvt_pk_bf16_f32 v14, v14, v15
	v_cvt_pk_bf16_f32 v15, v16, v17
	v_lshl_add_u64 v[18:19], v[78:79], 1, v[24:25]
	global_store_dwordx2 v[18:19], v[14:15], off offset:512
	global_load_dwordx4 v[14:17], v[22:23], off offset:64
	s_waitcnt vmcnt(0)
	v_mul_f32_e32 v10, v10, v14
	v_mul_f32_e32 v11, v11, v15
	v_mul_f32_e32 v12, v12, v16
	v_mul_f32_e32 v13, v13, v17
	v_cvt_pk_bf16_f32 v10, v10, v11
	v_cvt_pk_bf16_f32 v11, v12, v13
	global_store_dwordx2 v[18:19], v[10:11], off offset:544
	global_load_dwordx4 v[10:13], v[22:23], off offset:128
	s_waitcnt vmcnt(0)
	v_mul_f32_e32 v6, v6, v10
	v_mul_f32_e32 v7, v7, v11
	v_mul_f32_e32 v8, v8, v12
	v_mul_f32_e32 v9, v9, v13
	v_cvt_pk_bf16_f32 v6, v6, v7
	v_cvt_pk_bf16_f32 v7, v8, v9
	global_store_dwordx2 v[18:19], v[6:7], off offset:576
	global_load_dwordx4 v[6:9], v[22:23], off offset:192
	v_mov_b32_e32 v13, v115
	v_mov_b32_e32 v22, 0x3b800000
	s_waitcnt vmcnt(0)
	v_mul_f32_e32 v2, v2, v6
	v_mul_f32_e32 v3, v3, v7
	v_mul_f32_e32 v4, v4, v8
	v_mul_f32_e32 v5, v5, v9
	v_cvt_pk_bf16_f32 v2, v2, v3
	v_cvt_pk_bf16_f32 v3, v4, v5
	global_store_dwordx2 v[18:19], v[2:3], off offset:608
	v_add_u32_e32 v2, 0, v43
	v_lshlrev_b32_e32 v6, 2, v1
	v_lshl_add_u32 v1, v1, 4, 0
	ds_write2st64_b32 v2, v42, v32 offset1:4
	ds_write2st64_b32 v2, v33, v34 offset0:8 offset1:12
	ds_write2st64_b32 v2, v35, v36 offset0:16 offset1:20
	ds_write2st64_b32 v2, v37, v38 offset0:24 offset1:28
	ds_write2st64_b32 v2, v39, v40 offset0:32 offset1:36
	ds_write2st64_b32 v2, v41, v49 offset0:40 offset1:44
	ds_write2st64_b32 v2, v48, v47 offset0:48 offset1:52
	ds_write_b32 v2, v46 offset:14336
	v_add_u32_e32 v2, 0, v44
	v_lshl_add_u32 v8, s91, 12, v1
	ds_write_b32 v2, v45
	s_waitcnt lgkmcnt(0)
	s_barrier
	ds_read_b128 v[8:11], v8
	v_ashrrev_i32_e32 v7, 31, v6
	v_lshlrev_b64 v[2:3], 2, v[6:7]
	v_lshl_add_u64 v[4:5], s[76:77], 0, v[2:3]
	v_lshl_add_u64 v[2:3], s[14:15], 0, v[2:3]
	s_waitcnt lgkmcnt(0)
	v_add_f32_e32 v12, v8, v9
	v_add_f32_e32 v12, v10, v12
	v_add_f32_e32 v12, v11, v12
	v_lshlrev_b64 v[6:7], 1, v[6:7]
	s_nop 0
	v_add_f32_dpp v12, v12, v12 quad_perm:[1,0,3,2] row_mask:0xf bank_mask:0xf bound_ctrl:1
	s_nop 1
	v_add_f32_dpp v12, v12, v12 quad_perm:[2,3,0,1] row_mask:0xf bank_mask:0xf bound_ctrl:1
	s_nop 1
	v_add_f32_dpp v12, v12, v12 row_half_mirror row_mask:0xf bank_mask:0xf bound_ctrl:1
	s_nop 1
	v_add_f32_dpp v12, v12, v12 row_mirror row_mask:0xf bank_mask:0xf bound_ctrl:1
	s_nop 1
	v_mov_b32_dpp v13, v12 row_bcast:15 row_mask:0xa bank_mask:0xf
	v_add_f32_e32 v12, v12, v13
	v_mov_b32_e32 v13, v115
	s_nop 1
	v_mov_b32_dpp v13, v12 row_bcast:31 row_mask:0xc bank_mask:0xf
	v_add_f32_e32 v12, v12, v13
	s_nop 0
	v_readlane_b32 s1, v12, 63
	s_nop 1
	v_fmac_f32_e32 v9, s1, v250
	v_fma_f32 v17, s1, v250, v11
	v_fma_f32 v16, s1, v250, v10
	v_fma_f32 v8, s1, v250, v8
	v_mul_f32_e32 v12, v9, v9
	v_fmac_f32_e32 v12, v8, v8
	v_mul_f32_e32 v10, v16, v16
	v_mul_f32_e32 v11, v17, v17
	s_nop 0
	v_add_f32_e32 v10, v10, v12
	v_add_f32_e32 v10, v11, v10
	v_mov_b32_e32 v11, v115
	s_nop 0
	v_add_f32_dpp v10, v10, v10 quad_perm:[1,0,3,2] row_mask:0xf bank_mask:0xf bound_ctrl:1
	s_nop 1
	v_add_f32_dpp v10, v10, v10 quad_perm:[2,3,0,1] row_mask:0xf bank_mask:0xf bound_ctrl:1
	s_nop 1
	v_add_f32_dpp v10, v10, v10 row_half_mirror row_mask:0xf bank_mask:0xf bound_ctrl:1
	s_nop 1
	v_add_f32_dpp v10, v10, v10 row_mirror row_mask:0xf bank_mask:0xf bound_ctrl:1
	s_nop 1
	v_mov_b32_dpp v11, v10 row_bcast:15 row_mask:0xa bank_mask:0xf
	v_add_f32_e32 v10, v10, v11
	v_mov_b32_e32 v11, v115
	s_nop 1
	v_mov_b32_dpp v11, v10 row_bcast:31 row_mask:0xc bank_mask:0xf
	v_add_f32_e32 v10, v10, v11
	s_nop 0
	v_readlane_b32 s1, v10, 63
	s_nop 1
	v_fma_f32 v10, s1, v22, v225
	v_rsq_f32_e32 v18, v10
	s_or_b32 s1, s0, 1
	v_mul_f32_e32 v20, v8, v18
	v_mul_f32_e32 v21, v9, v18
	global_load_dwordx4 v[8:11], v[4:5], off
	global_load_dwordx4 v[12:15], v[2:3], off
	s_waitcnt vmcnt(0)
	v_fma_f32 v8, v8, v20, v12
	v_fma_f32 v9, v9, v21, v13
	s_nop 0
	v_mul_f32_e32 v12, 0xbfb8aa3b, v8
	v_mul_f32_e32 v13, 0xbfb8aa3b, v9
	v_exp_f32_e32 v12, v12
	v_exp_f32_e32 v13, v13
	v_add_f32_e32 v12, 1.0, v12
	v_add_f32_e32 v13, 1.0, v13
	v_rcp_f32_e32 v12, v12
	v_rcp_f32_e32 v13, v13
	s_nop 0
	v_mul_f32_e32 v8, v8, v12
	v_mul_f32_e32 v9, v9, v13
	v_mul_f32_e32 v12, v16, v18
	v_mul_f32_e32 v13, v17, v18
	v_cvt_pk_bf16_f32 v8, v8, v9
	v_fma_f32 v10, v12, v10, v14
	v_fma_f32 v11, v13, v11, v15
	s_nop 0
	v_mul_f32_e32 v12, 0xbfb8aa3b, v10
	v_mul_f32_e32 v13, 0xbfb8aa3b, v11
	v_exp_f32_e32 v12, v12
	v_exp_f32_e32 v13, v13
	v_add_f32_e32 v12, 1.0, v12
	v_add_f32_e32 v13, 1.0, v13
	v_rcp_f32_e32 v12, v12
	v_rcp_f32_e32 v13, v13
	s_nop 0
	v_mul_f32_e32 v10, v10, v12
	v_mul_f32_e32 v11, v11, v13
	s_nop 0
	v_cvt_pk_bf16_f32 v9, v10, v11
	v_lshl_add_u64 v[10:11], s[2:3], 0, v[6:7]
	global_store_dwordx2 v[10:11], v[8:9], off offset:1536
	v_lshl_add_u32 v8, s1, 10, v1
	ds_read_b128 v[12:15], v8
	v_mov_b32_e32 v9, v115
	s_waitcnt lgkmcnt(0)
	v_add_f32_e32 v8, v12, v13
	v_add_f32_e32 v8, v14, v8
	v_add_f32_e32 v8, v15, v8
	s_nop 1
	v_add_f32_dpp v8, v8, v8 quad_perm:[1,0,3,2] row_mask:0xf bank_mask:0xf bound_ctrl:1
	s_nop 1
	v_add_f32_dpp v8, v8, v8 quad_perm:[2,3,0,1] row_mask:0xf bank_mask:0xf bound_ctrl:1
	s_nop 1
	v_add_f32_dpp v8, v8, v8 row_half_mirror row_mask:0xf bank_mask:0xf bound_ctrl:1
	s_nop 1
	v_add_f32_dpp v8, v8, v8 row_mirror row_mask:0xf bank_mask:0xf bound_ctrl:1
	s_nop 1
	v_mov_b32_dpp v9, v8 row_bcast:15 row_mask:0xa bank_mask:0xf
	v_add_f32_e32 v8, v8, v9
	v_mov_b32_e32 v9, v115
	s_nop 1
	v_mov_b32_dpp v9, v8 row_bcast:31 row_mask:0xc bank_mask:0xf
	v_add_f32_e32 v8, v8, v9
	s_nop 0
	v_readlane_b32 s2, v8, 63
	s_nop 1
	v_fmac_f32_e32 v13, s2, v250
	v_fma_f32 v9, s2, v250, v15
	v_fma_f32 v8, s2, v250, v14
	v_fma_f32 v12, s2, v250, v12
	v_mul_f32_e32 v14, v13, v13
	v_fmac_f32_e32 v14, v12, v12
	v_mul_f32_e32 v10, v8, v8
	v_mul_f32_e32 v11, v9, v9
	s_nop 0
	v_add_f32_e32 v10, v10, v14
	global_load_dwordx4 v[14:17], v[4:5], off
	global_load_dwordx4 v[18:21], v[2:3], off
	v_add_f32_e32 v10, v11, v10
	v_mov_b32_e32 v11, v115
	s_nop 0
	v_add_f32_dpp v10, v10, v10 quad_perm:[1,0,3,2] row_mask:0xf bank_mask:0xf bound_ctrl:1
	s_nop 1
	v_add_f32_dpp v10, v10, v10 quad_perm:[2,3,0,1] row_mask:0xf bank_mask:0xf bound_ctrl:1
	s_nop 1
	v_add_f32_dpp v10, v10, v10 row_half_mirror row_mask:0xf bank_mask:0xf bound_ctrl:1
	s_nop 1
	v_add_f32_dpp v10, v10, v10 row_mirror row_mask:0xf bank_mask:0xf bound_ctrl:1
	s_nop 1
	v_mov_b32_dpp v11, v10 row_bcast:15 row_mask:0xa bank_mask:0xf
	v_add_f32_e32 v10, v10, v11
	v_mov_b32_e32 v11, v115
	s_nop 1
	v_mov_b32_dpp v11, v10 row_bcast:31 row_mask:0xc bank_mask:0xf
	v_add_f32_e32 v10, v10, v11
	s_nop 0
	v_readlane_b32 s2, v10, 63
	s_nop 1
	v_fma_f32 v10, s2, v22, v225
	v_rsq_f32_e32 v10, v10
	s_add_i32 s2, s1, s90
	s_ashr_i32 s3, s2, 31
	s_lshl_b64 s[2:3], s[2:3], 11
	v_mul_f32_e32 v12, v12, v10
	v_mul_f32_e32 v13, v13, v10
	s_add_u32 s2, s86, s2
	s_addc_u32 s3, s87, s3
	s_or_b32 s1, s0, 2
	s_waitcnt vmcnt(0)
	v_fma_f32 v12, v14, v12, v18
	v_fma_f32 v13, v15, v13, v19
	s_nop 0
	v_mul_f32_e32 v11, 0xbfb8aa3b, v12
	v_exp_f32_e32 v11, v11
	s_nop 0
	v_add_f32_e32 v11, 1.0, v11
	v_rcp_f32_e32 v14, v11
	v_mul_f32_e32 v11, 0xbfb8aa3b, v13
	v_exp_f32_e32 v11, v11
	s_nop 0
	v_add_f32_e32 v11, 1.0, v11
	v_mul_f32_e32 v8, v8, v10
	v_mul_f32_e32 v9, v9, v10
	v_rcp_f32_e32 v15, v11
	v_fma_f32 v8, v8, v16, v20
	v_fma_f32 v9, v9, v17, v21
	v_mul_f32_e32 v12, v12, v14
	v_mul_f32_e32 v13, v13, v15
	v_mul_f32_e32 v10, 0xbfb8aa3b, v8
	v_mul_f32_e32 v11, 0xbfb8aa3b, v9
	v_exp_f32_e32 v10, v10
	v_exp_f32_e32 v11, v11
	v_add_f32_e32 v10, 1.0, v10
	v_add_f32_e32 v11, 1.0, v11
	v_rcp_f32_e32 v10, v10
	v_rcp_f32_e32 v11, v11
	s_nop 0
	v_mul_f32_e32 v8, v8, v10
	v_mul_f32_e32 v9, v9, v11
	v_cvt_pk_bf16_f32 v10, v12, v13
	v_cvt_pk_bf16_f32 v11, v8, v9
	v_lshl_add_u64 v[8:9], s[2:3], 0, v[6:7]
	global_store_dwordx2 v[8:9], v[10:11], off offset:1536
	v_lshl_add_u32 v8, s1, 10, v1
	ds_read_b128 v[8:11], v8
	v_mov_b32_e32 v13, v115
	s_waitcnt lgkmcnt(0)
	v_add_f32_e32 v12, v8, v9
	v_add_f32_e32 v12, v10, v12
	v_add_f32_e32 v12, v11, v12
	s_nop 1
	v_add_f32_dpp v12, v12, v12 quad_perm:[1,0,3,2] row_mask:0xf bank_mask:0xf bound_ctrl:1
	s_nop 1
	v_add_f32_dpp v12, v12, v12 quad_perm:[2,3,0,1] row_mask:0xf bank_mask:0xf bound_ctrl:1
	s_nop 1
	v_add_f32_dpp v12, v12, v12 row_half_mirror row_mask:0xf bank_mask:0xf bound_ctrl:1
	s_nop 1
	v_add_f32_dpp v12, v12, v12 row_mirror row_mask:0xf bank_mask:0xf bound_ctrl:1
	s_nop 1
	v_mov_b32_dpp v13, v12 row_bcast:15 row_mask:0xa bank_mask:0xf
	v_add_f32_e32 v12, v12, v13
	v_mov_b32_e32 v13, v115
	s_nop 1
	v_mov_b32_dpp v13, v12 row_bcast:31 row_mask:0xc bank_mask:0xf
	v_add_f32_e32 v12, v12, v13
	s_nop 0
	v_readlane_b32 s2, v12, 63
	s_nop 1
	v_fmac_f32_e32 v9, s2, v250
	v_fma_f32 v17, s2, v250, v11
	v_fma_f32 v16, s2, v250, v10
	v_fma_f32 v8, s2, v250, v8
	v_mul_f32_e32 v12, v9, v9
	v_fmac_f32_e32 v12, v8, v8
	v_mul_f32_e32 v10, v16, v16
	v_mul_f32_e32 v11, v17, v17
	s_nop 0
	v_add_f32_e32 v10, v10, v12
	v_add_f32_e32 v10, v11, v10
	v_mov_b32_e32 v11, v115
	s_nop 0
	v_add_f32_dpp v10, v10, v10 quad_perm:[1,0,3,2] row_mask:0xf bank_mask:0xf bound_ctrl:1
	s_nop 1
	v_add_f32_dpp v10, v10, v10 quad_perm:[2,3,0,1] row_mask:0xf bank_mask:0xf bound_ctrl:1
	s_nop 1
	v_add_f32_dpp v10, v10, v10 row_half_mirror row_mask:0xf bank_mask:0xf bound_ctrl:1
	s_nop 1
	v_add_f32_dpp v10, v10, v10 row_mirror row_mask:0xf bank_mask:0xf bound_ctrl:1
	s_nop 1
	v_mov_b32_dpp v11, v10 row_bcast:15 row_mask:0xa bank_mask:0xf
	v_add_f32_e32 v10, v10, v11
	v_mov_b32_e32 v11, v115
	s_nop 1
	v_mov_b32_dpp v11, v10 row_bcast:31 row_mask:0xc bank_mask:0xf
	v_add_f32_e32 v10, v10, v11
	s_nop 0
	v_readlane_b32 s2, v10, 63
	s_nop 1
	v_fma_f32 v10, s2, v22, v225
	v_rsq_f32_e32 v18, v10
	s_add_i32 s2, s1, s90
	s_ashr_i32 s3, s2, 31
	s_lshl_b64 s[2:3], s[2:3], 11
	v_mul_f32_e32 v20, v8, v18
	v_mul_f32_e32 v21, v9, v18
	global_load_dwordx4 v[8:11], v[4:5], off
	global_load_dwordx4 v[12:15], v[2:3], off
	s_add_u32 s2, s86, s2
	s_addc_u32 s3, s87, s3
	s_or_b32 s0, s0, 3
	v_lshl_add_u32 v1, s0, 10, v1
	s_add_i32 s0, s0, s90
	s_waitcnt vmcnt(0)
	v_fma_f32 v8, v8, v20, v12
	v_fma_f32 v9, v9, v21, v13
	s_nop 0
	v_mul_f32_e32 v12, 0xbfb8aa3b, v8
	v_mul_f32_e32 v13, 0xbfb8aa3b, v9
	v_exp_f32_e32 v12, v12
	v_exp_f32_e32 v13, v13
	v_add_f32_e32 v12, 1.0, v12
	v_add_f32_e32 v13, 1.0, v13
	v_rcp_f32_e32 v12, v12
	v_rcp_f32_e32 v13, v13
	s_nop 0
	v_mul_f32_e32 v8, v8, v12
	v_mul_f32_e32 v9, v9, v13
	v_mul_f32_e32 v12, v16, v18
	v_mul_f32_e32 v13, v17, v18
	v_cvt_pk_bf16_f32 v8, v8, v9
	v_fma_f32 v10, v12, v10, v14
	v_fma_f32 v11, v13, v11, v15
	s_nop 0
	v_mul_f32_e32 v12, 0xbfb8aa3b, v10
	v_mul_f32_e32 v13, 0xbfb8aa3b, v11
	v_exp_f32_e32 v12, v12
	v_exp_f32_e32 v13, v13
	v_add_f32_e32 v12, 1.0, v12
	v_add_f32_e32 v13, 1.0, v13
	v_rcp_f32_e32 v12, v12
	v_rcp_f32_e32 v13, v13
	s_nop 0
	v_mul_f32_e32 v10, v10, v12
	v_mul_f32_e32 v11, v11, v13
	ds_read_b128 v[12:15], v1
	v_cvt_pk_bf16_f32 v9, v10, v11
	v_lshl_add_u64 v[10:11], s[2:3], 0, v[6:7]
	global_store_dwordx2 v[10:11], v[8:9], off offset:1536
	v_mov_b32_e32 v8, v115
	s_waitcnt lgkmcnt(0)
	v_add_f32_e32 v1, v12, v13
	v_add_f32_e32 v1, v14, v1
	v_add_f32_e32 v1, v15, v1
	s_nop 1
	v_add_f32_dpp v1, v1, v1 quad_perm:[1,0,3,2] row_mask:0xf bank_mask:0xf bound_ctrl:1
	s_nop 1
	v_add_f32_dpp v1, v1, v1 quad_perm:[2,3,0,1] row_mask:0xf bank_mask:0xf bound_ctrl:1
	s_nop 1
	v_add_f32_dpp v1, v1, v1 row_half_mirror row_mask:0xf bank_mask:0xf bound_ctrl:1
	s_nop 1
	v_add_f32_dpp v1, v1, v1 row_mirror row_mask:0xf bank_mask:0xf bound_ctrl:1
	s_nop 1
	v_mov_b32_dpp v8, v1 row_bcast:15 row_mask:0xa bank_mask:0xf
	v_add_f32_e32 v1, v1, v8
	v_mov_b32_e32 v8, v115
	s_nop 1
	v_mov_b32_dpp v8, v1 row_bcast:31 row_mask:0xc bank_mask:0xf
	v_add_f32_e32 v1, v1, v8
	s_nop 0
	v_readlane_b32 s1, v1, 63
	s_nop 1
	v_fma_f32 v9, s1, v250, v15
	v_fma_f32 v8, s1, v250, v14
	global_load_dwordx4 v[14:17], v[4:5], off
	s_nop 0
	global_load_dwordx4 v[2:5], v[2:3], off
	v_fmac_f32_e32 v13, s1, v250
	v_fma_f32 v12, s1, v250, v12
	v_mul_f32_e32 v1, v13, v13
	v_fmac_f32_e32 v1, v12, v12
	v_mul_f32_e32 v10, v8, v8
	v_mul_f32_e32 v11, v9, v9
	s_nop 0
	v_add_f32_e32 v1, v10, v1
	v_add_f32_e32 v1, v11, v1
	v_mov_b32_e32 v10, v115
	s_nop 0
	v_add_f32_dpp v1, v1, v1 quad_perm:[1,0,3,2] row_mask:0xf bank_mask:0xf bound_ctrl:1
	s_nop 1
	v_add_f32_dpp v1, v1, v1 quad_perm:[2,3,0,1] row_mask:0xf bank_mask:0xf bound_ctrl:1
	s_nop 1
	v_add_f32_dpp v1, v1, v1 row_half_mirror row_mask:0xf bank_mask:0xf bound_ctrl:1
	s_nop 1
	v_add_f32_dpp v1, v1, v1 row_mirror row_mask:0xf bank_mask:0xf bound_ctrl:1
	s_nop 1
	v_mov_b32_dpp v10, v1 row_bcast:15 row_mask:0xa bank_mask:0xf
	v_add_f32_e32 v1, v1, v10
	v_mov_b32_e32 v10, v115
	s_nop 1
	v_mov_b32_dpp v10, v1 row_bcast:31 row_mask:0xc bank_mask:0xf
	v_add_f32_e32 v1, v1, v10
	s_nop 0
	v_readlane_b32 s1, v1, 63
	s_nop 1
	v_fma_f32 v1, s1, v22, v225
	v_rsq_f32_e32 v10, v1
	s_ashr_i32 s1, s0, 31
	s_lshl_b64 s[0:1], s[0:1], 11
	s_add_u32 s0, s86, s0
	v_mul_f32_e32 v12, v12, v10
	v_mul_f32_e32 v13, v13, v10
	v_mul_f32_e32 v8, v8, v10
	v_mul_f32_e32 v9, v9, v10
	s_addc_u32 s1, s87, s1
	s_add_i32 s55, s55, s94
	s_cmpk_gt_i32 s55, 0x3ff
	s_waitcnt vmcnt(0)
	v_fma_f32 v2, v14, v12, v2
	v_fma_f32 v3, v15, v13, v3
	s_nop 0
	v_mul_f32_e32 v1, 0xbfb8aa3b, v2
	v_exp_f32_e32 v1, v1
	v_fma_f32 v4, v8, v16, v4
	v_fma_f32 v5, v9, v17, v5
	v_add_f32_e32 v1, 1.0, v1
	v_rcp_f32_e32 v12, v1
	v_mul_f32_e32 v1, 0xbfb8aa3b, v3
	v_exp_f32_e32 v1, v1
	s_nop 0
	v_add_f32_e32 v1, 1.0, v1
	v_rcp_f32_e32 v13, v1
	v_mul_f32_e32 v1, 0xbfb8aa3b, v4
	v_exp_f32_e32 v1, v1
	v_mul_f32_e32 v2, v2, v12
	v_mul_f32_e32 v3, v3, v13
	s_nop 0
	v_cvt_pk_bf16_f32 v2, v2, v3
	v_add_f32_e32 v1, 1.0, v1
	v_rcp_f32_e32 v8, v1
	v_mul_f32_e32 v1, 0xbfb8aa3b, v5
	v_exp_f32_e32 v1, v1
	s_nop 0
	v_add_f32_e32 v1, 1.0, v1
	v_rcp_f32_e32 v9, v1
	s_nop 0
	v_mul_f32_e32 v4, v4, v8
	v_mul_f32_e32 v5, v5, v9
	s_nop 0
	v_cvt_pk_bf16_f32 v3, v4, v5
	v_lshl_add_u64 v[4:5], s[0:1], 0, v[6:7]
	global_store_dwordx2 v[4:5], v[2:3], off offset:1536
	s_barrier
	s_cbranch_scc0 .LBB0_367
	s_branch .LBB0_412
.LBB0_409:
	v_lshlrev_b32_e32 v34, 16, v46
	v_and_b32_e32 v35, 0xffff0000, v46
	v_mul_f32_e32 v34, 0xbfb8aa3b, v34
	v_mul_f32_e32 v35, 0xbfb8aa3b, v35
	v_exp_f32_e32 v34, v34
	v_exp_f32_e32 v35, v35
	v_lshlrev_b32_e32 v38, 16, v47
	v_lshlrev_b32_e32 v36, 16, v22
	v_and_b32_e32 v37, 0xffff0000, v22
	v_mul_f32_e32 v22, 0xbfb8aa3b, v38
	v_add_f32_e32 v34, 1.0, v34
	v_add_f32_e32 v35, 1.0, v35
	v_exp_f32_e32 v22, v22
	v_rcp_f32_e32 v34, v34
	v_rcp_f32_e32 v35, v35
	v_and_b32_e32 v39, 0xffff0000, v47
	v_add_f32_e32 v22, 1.0, v22
	v_lshlrev_b32_e32 v40, 16, v48
	v_mul_f32_e32 v34, v34, v36
	v_mul_f32_e32 v35, v35, v37
	v_rcp_f32_e32 v36, v22
	v_mul_f32_e32 v22, 0xbfb8aa3b, v39
	v_exp_f32_e32 v22, v22
	v_and_b32_e32 v41, 0xffff0000, v48
	v_lshlrev_b32_e32 v42, 16, v49
	v_lshlrev_b32_e32 v38, 16, v24
	v_add_f32_e32 v22, 1.0, v22
	v_rcp_f32_e32 v37, v22
	v_lshlrev_b32_e32 v22, 16, v23
	v_and_b32_e32 v23, 0xffff0000, v23
	v_and_b32_e32 v39, 0xffff0000, v24
	v_mul_f32_e32 v36, v36, v22
	v_mul_f32_e32 v37, v37, v23
	v_mul_f32_e32 v22, 0xbfb8aa3b, v40
	v_mul_f32_e32 v23, 0xbfb8aa3b, v41
	v_exp_f32_e32 v22, v22
	v_exp_f32_e32 v23, v23
	v_mul_f32_e32 v24, 0xbfb8aa3b, v42
	v_exp_f32_e32 v24, v24
	v_add_f32_e32 v22, 1.0, v22
	v_add_f32_e32 v23, 1.0, v23
	v_rcp_f32_e32 v22, v22
	v_rcp_f32_e32 v23, v23
	v_and_b32_e32 v43, 0xffff0000, v49
	v_add_f32_e32 v24, 1.0, v24
	v_lshl_add_u32 v33, v33, 2, v30
	v_mul_f32_e32 v22, v22, v38
	v_mul_f32_e32 v23, v23, v39
	v_rcp_f32_e32 v38, v24
	v_mul_f32_e32 v24, 0xbfb8aa3b, v43
	v_exp_f32_e32 v24, v24
	s_nop 0
	v_add_f32_e32 v24, 1.0, v24
	v_rcp_f32_e32 v39, v24
	v_lshlrev_b32_e32 v24, 16, v25
	v_and_b32_e32 v25, 0xffff0000, v25
	v_mul_f32_e32 v24, v38, v24
	v_mul_f32_e32 v25, v39, v25
	ds_write_b128 v33, v[34:37]
	ds_write_b128 v33, v[22:25] offset:16
	s_or_b64 exec, exec, s[18:19]
	s_and_saveexec_b64 s[18:19], s[38:39]
	s_cbranch_execz .LBB0_397
.LBB0_410:
	v_lshlrev_b32_e32 v22, 16, v26
	v_and_b32_e32 v23, 0xffff0000, v26
	v_mul_f32_e32 v22, 0xbfb8aa3b, v22
	v_mul_f32_e32 v23, 0xbfb8aa3b, v23
	v_exp_f32_e32 v22, v22
	v_exp_f32_e32 v23, v23
	v_lshlrev_b32_e32 v26, 16, v27
	v_lshlrev_b32_e32 v24, 16, v14
	v_and_b32_e32 v25, 0xffff0000, v14
	v_mul_f32_e32 v14, 0xbfb8aa3b, v26
	v_add_f32_e32 v22, 1.0, v22
	v_add_f32_e32 v23, 1.0, v23
	v_exp_f32_e32 v14, v14
	v_rcp_f32_e32 v22, v22
	v_rcp_f32_e32 v23, v23
	v_and_b32_e32 v27, 0xffff0000, v27
	v_add_f32_e32 v14, 1.0, v14
	v_lshlrev_b32_e32 v33, 16, v28
	v_mul_f32_e32 v22, v22, v24
	v_mul_f32_e32 v23, v23, v25
	v_rcp_f32_e32 v24, v14
	v_mul_f32_e32 v14, 0xbfb8aa3b, v27
	v_exp_f32_e32 v14, v14
	v_and_b32_e32 v28, 0xffff0000, v28
	v_lshlrev_b32_e32 v34, 16, v29
	v_lshlrev_b32_e32 v26, 16, v16
	v_add_f32_e32 v14, 1.0, v14
	v_rcp_f32_e32 v25, v14
	v_lshlrev_b32_e32 v14, 16, v15
	v_and_b32_e32 v15, 0xffff0000, v15
	v_and_b32_e32 v27, 0xffff0000, v16
	v_mul_f32_e32 v24, v24, v14
	v_mul_f32_e32 v25, v25, v15
	v_mul_f32_e32 v14, 0xbfb8aa3b, v33
	v_mul_f32_e32 v15, 0xbfb8aa3b, v28
	v_exp_f32_e32 v14, v14
	v_exp_f32_e32 v15, v15
	v_mul_f32_e32 v16, 0xbfb8aa3b, v34
	v_exp_f32_e32 v16, v16
	v_add_f32_e32 v14, 1.0, v14
	v_add_f32_e32 v15, 1.0, v15
	v_rcp_f32_e32 v14, v14
	v_rcp_f32_e32 v15, v15
	v_and_b32_e32 v29, 0xffff0000, v29
	v_add_f32_e32 v16, 1.0, v16
	v_mul_f32_e32 v14, v14, v26
	v_mul_f32_e32 v15, v15, v27
	v_rcp_f32_e32 v26, v16
	v_mul_f32_e32 v16, 0xbfb8aa3b, v29
	v_exp_f32_e32 v16, v16
	s_nop 0
	v_add_f32_e32 v16, 1.0, v16
	v_rcp_f32_e32 v27, v16
	v_lshlrev_b32_e32 v16, 16, v17
	v_and_b32_e32 v17, 0xffff0000, v17
	v_mul_f32_e32 v16, v26, v16
	v_mul_f32_e32 v17, v27, v17
	v_add_u32_e32 v26, v30, v32
	ds_write_b128 v26, v[22:25]
	ds_write_b128 v26, v[14:17] offset:16
	s_or_b64 exec, exec, s[18:19]
	s_and_saveexec_b64 s[18:19], s[0:1]
	s_cbranch_execz .LBB0_398
.LBB0_411:
	v_lshlrev_b32_e32 v14, 16, v18
	v_and_b32_e32 v15, 0xffff0000, v18
	v_mul_f32_e32 v14, 0xbfb8aa3b, v14
	v_mul_f32_e32 v15, 0xbfb8aa3b, v15
	v_exp_f32_e32 v14, v14
	v_exp_f32_e32 v15, v15
	v_lshlrev_b32_e32 v18, 16, v19
	v_lshlrev_b32_e32 v16, 16, v6
	v_and_b32_e32 v17, 0xffff0000, v6
	v_mul_f32_e32 v6, 0xbfb8aa3b, v18
	v_add_f32_e32 v14, 1.0, v14
	v_add_f32_e32 v15, 1.0, v15
	v_exp_f32_e32 v6, v6
	v_rcp_f32_e32 v14, v14
	v_rcp_f32_e32 v15, v15
	v_and_b32_e32 v19, 0xffff0000, v19
	v_add_f32_e32 v6, 1.0, v6
	v_lshlrev_b32_e32 v22, 16, v20
	v_mul_f32_e32 v14, v14, v16
	v_mul_f32_e32 v15, v15, v17
	v_rcp_f32_e32 v16, v6
	v_mul_f32_e32 v6, 0xbfb8aa3b, v19
	v_exp_f32_e32 v6, v6
	v_and_b32_e32 v20, 0xffff0000, v20
	v_lshlrev_b32_e32 v23, 16, v21
	v_lshlrev_b32_e32 v18, 16, v8
	v_add_f32_e32 v6, 1.0, v6
	v_rcp_f32_e32 v17, v6
	v_lshlrev_b32_e32 v6, 16, v7
	v_and_b32_e32 v7, 0xffff0000, v7
	v_and_b32_e32 v19, 0xffff0000, v8
	v_mul_f32_e32 v16, v16, v6
	v_mul_f32_e32 v17, v17, v7
	v_mul_f32_e32 v6, 0xbfb8aa3b, v22
	v_mul_f32_e32 v7, 0xbfb8aa3b, v20
	v_exp_f32_e32 v6, v6
	v_exp_f32_e32 v7, v7
	v_mul_f32_e32 v8, 0xbfb8aa3b, v23
	v_exp_f32_e32 v8, v8
	v_add_f32_e32 v6, 1.0, v6
	v_add_f32_e32 v7, 1.0, v7
	v_rcp_f32_e32 v6, v6
	v_rcp_f32_e32 v7, v7
	v_and_b32_e32 v21, 0xffff0000, v21
	v_add_f32_e32 v8, 1.0, v8
	v_mul_f32_e32 v6, v6, v18
	v_mul_f32_e32 v7, v7, v19
	v_rcp_f32_e32 v18, v8
	v_mul_f32_e32 v8, 0xbfb8aa3b, v21
	v_exp_f32_e32 v8, v8
	s_nop 0
	v_add_f32_e32 v8, 1.0, v8
	v_rcp_f32_e32 v19, v8
	v_lshlrev_b32_e32 v8, 16, v9
	v_and_b32_e32 v9, 0xffff0000, v9
	v_mul_f32_e32 v8, v18, v8
	v_mul_f32_e32 v9, v19, v9
	v_add_u32_e32 v18, v30, v31
	ds_write_b128 v18, v[14:17]
	ds_write_b128 v18, v[6:9] offset:16
	s_or_b64 exec, exec, s[18:19]
	s_and_saveexec_b64 s[0:1], vcc
	s_cbranch_execnz .LBB0_399
	s_branch .LBB0_400
